# gate-logit arrays stored and read in MFMA fragment order (coalesced 512-byte wave accesses) between the in-proj epilogue and the mix GEMM hooks; canonicalising v_max folded into v_med3 in the mix hook
# speedup vs baseline: 1.0231x; 1.0111x over previous
.LBB0_223:
	s_ashr_i32 s7, s4, 31
	v_readlane_b32 s29, v253, 35
	s_add_u32 s29, s29, s4
	v_readlane_b32 s33, v253, 37
	s_addc_u32 s7, s33, s7
	v_readlane_b32 s33, v253, 39
	s_add_u32 s33, s33, s4
	v_readlane_b32 s57, v253, 41
	s_addc_u32 s57, s57, 0
	s_add_u32 s33, s33, 0xfffffc00
	s_addc_u32 s57, s57, -1
	v_pk_mul_f32 v[10:11], v[158:159], s[12:13] op_sel_hi:[1,0]
	s_cmp_lt_i32 s76, 4
	v_med3_f32 v16, v10, s52, v175
	v_med3_f32 v11, v11, s52, v175
	v_mov_b32_e32 v10, 0
	s_cselect_b32 s79, s7, s57
	s_cselect_b32 s78, s29, s33
	v_cvt_pk_fp8_f32 v10, v16, v11
	v_lshl_add_u64 v[6:7], s[78:79], 0, v[4:5]
	v_lshlrev_b64 v[8:9], 10, v[2:3]
	v_lshl_add_u64 v[6:7], v[6:7], 0, v[8:9]
	v_lshrrev_b32_e32 v214, 6, v0
	v_lshlrev_b32_e32 v214, 13, v214
	v_and_b32_e32 v215, 63, v0
	v_lshl_add_u32 v214, v215, 3, v214
	v_lshrrev_b32_e32 v215, 8, v2
	v_lshl_add_u32 v214, v215, 18, v214
	s_sub_i32 s32, s4, 0x400
	s_cmp_lt_i32 s76, 4
	s_cselect_b32 s32, s4, s32
	s_mulk_i32 s32, 0xff
	v_add_u32_e32 v214, s32, v214
	v_mov_b32_e32 v215, 0
	v_lshl_add_u64 v[220:221], s[78:79], 0, v[214:215]
	v_add_co_u32_e32 v222, vcc, 0x1000, v220
	s_nop 1
	v_addc_co_u32_e32 v223, vcc, 0, v221, vcc
	v_pk_mul_f32 v[8:9], v[160:161], s[12:13] op_sel_hi:[1,0]
	v_pk_mul_f32 v[14:15], v[154:155], s[12:13] op_sel_hi:[1,0]
	v_med3_f32 v8, v8, s52, v175
	v_med3_f32 v9, v9, s52, v175
	v_cvt_pk_fp8_f32 v10, v8, v9 op_sel:[0,0,1]
	v_med3_f32 v8, v14, s52, v175
	v_med3_f32 v9, v15, s52, v175
	v_mov_b32_e32 v11, 0
	v_cvt_pk_fp8_f32 v11, v8, v9
	v_pk_mul_f32 v[12:13], v[156:157], s[12:13] op_sel_hi:[1,0]
	v_pk_mul_f32 v[14:15], v[142:143], s[12:13] op_sel_hi:[1,0]
	v_med3_f32 v8, v12, s52, v175
	v_med3_f32 v9, v13, s52, v175
	v_cvt_pk_fp8_f32 v11, v8, v9 op_sel:[0,0,1]
	v_pk_mul_f32 v[8:9], v[152:153], s[12:13] op_sel_hi:[1,0]
	v_pk_mul_f32 v[12:13], v[144:145], s[12:13] op_sel_hi:[1,0]
	v_med3_f32 v8, v8, s52, v175
	global_store_dwordx2 v[220:221], v[10:11], off
	v_pk_mul_f32 v[10:11], v[150:151], s[12:13] op_sel_hi:[1,0]
	v_med3_f32 v9, v9, s52, v175
	v_med3_f32 v16, v10, s52, v175
	v_med3_f32 v11, v11, s52, v175
	v_mov_b32_e32 v10, 0
	v_cvt_pk_fp8_f32 v10, v16, v11
	v_mov_b32_e32 v11, 0
	v_pk_mul_f32 v[16:17], v[138:139], s[12:13] op_sel_hi:[1,0]
	s_movk_i32 s7, 0x4000
	v_cvt_pk_fp8_f32 v10, v8, v9 op_sel:[0,0,1]
	v_med3_f32 v8, v14, s52, v175
	v_med3_f32 v9, v15, s52, v175
	v_cvt_pk_fp8_f32 v11, v8, v9
	v_med3_f32 v8, v12, s52, v175
	v_med3_f32 v9, v13, s52, v175
	v_pk_mul_f32 v[12:13], v[146:147], s[12:13] op_sel_hi:[1,0]
	v_cvt_pk_fp8_f32 v11, v8, v9 op_sel:[0,0,1]
	v_med3_f32 v18, v12, s52, v175
	v_med3_f32 v13, v13, s52, v175
	v_mov_b32_e32 v12, 0
	v_cvt_pk_fp8_f32 v12, v18, v13
	global_store_dwordx2 v[220:221], v[10:11], off offset:512
	v_pk_mul_f32 v[10:11], v[148:149], s[12:13] op_sel_hi:[1,0]
	v_mov_b32_e32 v13, 0
	v_med3_f32 v10, v10, s52, v175
	v_med3_f32 v11, v11, s52, v175
	v_cvt_pk_fp8_f32 v12, v10, v11 op_sel:[0,0,1]
	v_med3_f32 v10, v16, s52, v175
	v_med3_f32 v11, v17, s52, v175
	v_cvt_pk_fp8_f32 v13, v10, v11
	v_pk_mul_f32 v[14:15], v[140:141], s[12:13] op_sel_hi:[1,0]
	v_pk_mul_f32 v[16:17], v[126:127], s[12:13] op_sel_hi:[1,0]
	v_med3_f32 v10, v14, s52, v175
	v_med3_f32 v11, v15, s52, v175
	v_cvt_pk_fp8_f32 v13, v10, v11 op_sel:[0,0,1]
	v_add_co_u32_e32 v10, vcc, s7, v6
	v_pk_mul_f32 v[14:15], v[128:129], s[12:13] op_sel_hi:[1,0]
	s_nop 0
	v_addc_co_u32_e32 v11, vcc, 0, v7, vcc
	global_store_dwordx2 v[220:221], v[12:13], off offset:1024
	v_pk_mul_f32 v[12:13], v[134:135], s[12:13] op_sel_hi:[1,0]
	v_pk_mul_f32 v[10:11], v[136:137], s[12:13] op_sel_hi:[1,0]
	v_med3_f32 v18, v12, s52, v175
	v_med3_f32 v13, v13, s52, v175
	v_mov_b32_e32 v12, 0
	v_cvt_pk_fp8_f32 v12, v18, v13
	v_med3_f32 v10, v10, s52, v175
	v_med3_f32 v11, v11, s52, v175
	v_mov_b32_e32 v13, 0
	v_cvt_pk_fp8_f32 v12, v10, v11 op_sel:[0,0,1]
	v_med3_f32 v10, v16, s52, v175
	v_med3_f32 v11, v17, s52, v175
	v_cvt_pk_fp8_f32 v13, v10, v11
	v_med3_f32 v10, v14, s52, v175
	v_med3_f32 v11, v15, s52, v175
	v_lshl_add_u64 v[8:9], v[6:7], 0, s[14:15]
	v_cvt_pk_fp8_f32 v13, v10, v11 op_sel:[0,0,1]
	v_pk_mul_f32 v[10:11], v[132:133], s[12:13] op_sel_hi:[1,0]
	v_pk_mul_f32 v[16:17], v[122:123], s[12:13] op_sel_hi:[1,0]
	v_med3_f32 v10, v10, s52, v175
	global_store_dwordx2 v[220:221], v[12:13], off offset:1536
	v_pk_mul_f32 v[12:13], v[130:131], s[12:13] op_sel_hi:[1,0]
	v_med3_f32 v11, v11, s52, v175
	v_med3_f32 v18, v12, s52, v175
	v_med3_f32 v13, v13, s52, v175
	v_mov_b32_e32 v12, 0
	v_cvt_pk_fp8_f32 v12, v18, v13
	v_mov_b32_e32 v13, 0
	v_pk_mul_f32 v[14:15], v[124:125], s[12:13] op_sel_hi:[1,0]
	s_mov_b32 s7, 0x8000
	v_cvt_pk_fp8_f32 v12, v10, v11 op_sel:[0,0,1]
	v_med3_f32 v10, v16, s52, v175
	v_med3_f32 v11, v17, s52, v175
	v_cvt_pk_fp8_f32 v13, v10, v11
	v_med3_f32 v10, v14, s52, v175
	v_med3_f32 v11, v15, s52, v175
	v_pk_mul_f32 v[16:17], v[110:111], s[12:13] op_sel_hi:[1,0]
	v_cvt_pk_fp8_f32 v13, v10, v11 op_sel:[0,0,1]
	v_add_co_u32_e32 v10, vcc, s7, v6
	v_pk_mul_f32 v[14:15], v[112:113], s[12:13] op_sel_hi:[1,0]
	s_nop 0
	v_addc_co_u32_e32 v11, vcc, 0, v7, vcc
	global_store_dwordx2 v[220:221], v[12:13], off offset:2048
	v_pk_mul_f32 v[12:13], v[118:119], s[12:13] op_sel_hi:[1,0]
	v_pk_mul_f32 v[10:11], v[120:121], s[12:13] op_sel_hi:[1,0]
	v_med3_f32 v18, v12, s52, v175
	v_med3_f32 v13, v13, s52, v175
	v_mov_b32_e32 v12, 0
	v_cvt_pk_fp8_f32 v12, v18, v13
	v_med3_f32 v10, v10, s52, v175
	v_med3_f32 v11, v11, s52, v175
	v_mov_b32_e32 v13, 0
	v_cvt_pk_fp8_f32 v12, v10, v11 op_sel:[0,0,1]
	v_med3_f32 v10, v16, s52, v175
	v_med3_f32 v11, v17, s52, v175
	v_cvt_pk_fp8_f32 v13, v10, v11
	v_med3_f32 v10, v14, s52, v175
	v_med3_f32 v11, v15, s52, v175
	v_lshl_add_u64 v[8:9], v[6:7], 0, s[16:17]
	v_cvt_pk_fp8_f32 v13, v10, v11 op_sel:[0,0,1]
	v_pk_mul_f32 v[10:11], v[116:117], s[12:13] op_sel_hi:[1,0]
	v_pk_mul_f32 v[16:17], v[106:107], s[12:13] op_sel_hi:[1,0]
	v_med3_f32 v10, v10, s52, v175
	global_store_dwordx2 v[220:221], v[12:13], off offset:2560
	v_pk_mul_f32 v[12:13], v[114:115], s[12:13] op_sel_hi:[1,0]
	v_med3_f32 v11, v11, s52, v175
	v_med3_f32 v18, v12, s52, v175
	v_med3_f32 v13, v13, s52, v175
	v_mov_b32_e32 v12, 0
	v_cvt_pk_fp8_f32 v12, v18, v13
	v_mov_b32_e32 v13, 0
	v_pk_mul_f32 v[14:15], v[108:109], s[12:13] op_sel_hi:[1,0]
	v_lshl_add_u64 v[8:9], v[6:7], 0, s[18:19]
	v_cvt_pk_fp8_f32 v12, v10, v11 op_sel:[0,0,1]
	v_med3_f32 v10, v16, s52, v175
	v_med3_f32 v11, v17, s52, v175
	v_cvt_pk_fp8_f32 v13, v10, v11
	v_med3_f32 v10, v14, s52, v175
	v_med3_f32 v11, v15, s52, v175
	v_pk_mul_f32 v[16:17], v[98:99], s[12:13] op_sel_hi:[1,0]
	v_cvt_pk_fp8_f32 v13, v10, v11 op_sel:[0,0,1]
	v_add_co_u32_e32 v10, vcc, s96, v6
	v_pk_mul_f32 v[14:15], v[100:101], s[12:13] op_sel_hi:[1,0]
	s_nop 0
	v_addc_co_u32_e32 v11, vcc, 0, v7, vcc
	global_store_dwordx2 v[220:221], v[12:13], off offset:3072
	v_pk_mul_f32 v[12:13], v[102:103], s[12:13] op_sel_hi:[1,0]
	v_pk_mul_f32 v[10:11], v[104:105], s[12:13] op_sel_hi:[1,0]
	v_med3_f32 v18, v12, s52, v175
	v_med3_f32 v13, v13, s52, v175
	v_mov_b32_e32 v12, 0
	v_cvt_pk_fp8_f32 v12, v18, v13
	v_med3_f32 v10, v10, s52, v175
	v_med3_f32 v11, v11, s52, v175
	v_mov_b32_e32 v13, 0
	v_cvt_pk_fp8_f32 v12, v10, v11 op_sel:[0,0,1]
	v_med3_f32 v10, v16, s52, v175
	v_med3_f32 v11, v17, s52, v175
	v_cvt_pk_fp8_f32 v13, v10, v11
	v_med3_f32 v10, v14, s52, v175
	v_med3_f32 v11, v15, s52, v175
	v_pk_mul_f32 v[16:17], v[90:91], s[12:13] op_sel_hi:[1,0]
	v_cvt_pk_fp8_f32 v13, v10, v11 op_sel:[0,0,1]
	v_pk_mul_f32 v[10:11], v[96:97], s[12:13] op_sel_hi:[1,0]
	v_pk_mul_f32 v[14:15], v[92:93], s[12:13] op_sel_hi:[1,0]
	v_med3_f32 v10, v10, s52, v175
	global_store_dwordx2 v[220:221], v[12:13], off offset:3584
	v_pk_mul_f32 v[12:13], v[94:95], s[12:13] op_sel_hi:[1,0]
	v_med3_f32 v11, v11, s52, v175
	v_med3_f32 v18, v12, s52, v175
	v_med3_f32 v13, v13, s52, v175
	v_mov_b32_e32 v12, 0
	v_cvt_pk_fp8_f32 v12, v18, v13
	v_mov_b32_e32 v13, 0
	s_mov_b64 s[78:79], 0x20000
	v_lshl_add_u64 v[8:9], v[6:7], 0, s[78:79]
	v_cvt_pk_fp8_f32 v12, v10, v11 op_sel:[0,0,1]
	v_med3_f32 v10, v16, s52, v175
	v_med3_f32 v11, v17, s52, v175
	v_cvt_pk_fp8_f32 v13, v10, v11
	v_med3_f32 v10, v14, s52, v175
	v_med3_f32 v11, v15, s52, v175
	v_pk_mul_f32 v[16:17], v[78:79], s[12:13] op_sel_hi:[1,0]
	v_cvt_pk_fp8_f32 v13, v10, v11 op_sel:[0,0,1]
	v_add_co_u32_e32 v10, vcc, s53, v6
	v_pk_mul_f32 v[14:15], v[80:81], s[12:13] op_sel_hi:[1,0]
	s_nop 0
	v_addc_co_u32_e32 v11, vcc, 0, v7, vcc
	global_store_dwordx2 v[222:223], v[12:13], off
	v_pk_mul_f32 v[12:13], v[86:87], s[12:13] op_sel_hi:[1,0]
	v_pk_mul_f32 v[10:11], v[88:89], s[12:13] op_sel_hi:[1,0]
	v_med3_f32 v18, v12, s52, v175
	v_med3_f32 v13, v13, s52, v175
	v_mov_b32_e32 v12, 0
	v_cvt_pk_fp8_f32 v12, v18, v13
	v_med3_f32 v10, v10, s52, v175
	v_med3_f32 v11, v11, s52, v175
	v_mov_b32_e32 v13, 0
	v_cvt_pk_fp8_f32 v12, v10, v11 op_sel:[0,0,1]
	v_med3_f32 v10, v16, s52, v175
	v_med3_f32 v11, v17, s52, v175
	v_cvt_pk_fp8_f32 v13, v10, v11
	v_med3_f32 v10, v14, s52, v175
	v_med3_f32 v11, v15, s52, v175
	v_pk_mul_f32 v[16:17], v[74:75], s[12:13] op_sel_hi:[1,0]
	v_cvt_pk_fp8_f32 v13, v10, v11 op_sel:[0,0,1]
	v_pk_mul_f32 v[10:11], v[84:85], s[12:13] op_sel_hi:[1,0]
	v_pk_mul_f32 v[14:15], v[76:77], s[12:13] op_sel_hi:[1,0]
	v_med3_f32 v10, v10, s52, v175
	global_store_dwordx2 v[222:223], v[12:13], off offset:512
	v_pk_mul_f32 v[12:13], v[82:83], s[12:13] op_sel_hi:[1,0]
	v_med3_f32 v11, v11, s52, v175
	v_med3_f32 v18, v12, s52, v175
	v_med3_f32 v13, v13, s52, v175
	v_mov_b32_e32 v12, 0
	v_cvt_pk_fp8_f32 v12, v18, v13
	v_mov_b32_e32 v13, 0
	v_lshl_add_u64 v[8:9], v[6:7], 0, s[20:21]
	v_cvt_pk_fp8_f32 v12, v10, v11 op_sel:[0,0,1]
	v_med3_f32 v10, v16, s52, v175
	v_med3_f32 v11, v17, s52, v175
	v_cvt_pk_fp8_f32 v13, v10, v11
	v_med3_f32 v10, v14, s52, v175
	v_med3_f32 v11, v15, s52, v175
	v_pk_mul_f32 v[16:17], v[62:63], s[12:13] op_sel_hi:[1,0]
	v_cvt_pk_fp8_f32 v13, v10, v11 op_sel:[0,0,1]
	v_add_co_u32_e32 v10, vcc, s64, v6
	v_pk_mul_f32 v[14:15], v[64:65], s[12:13] op_sel_hi:[1,0]
	s_nop 0
	v_addc_co_u32_e32 v11, vcc, 0, v7, vcc
	global_store_dwordx2 v[222:223], v[12:13], off offset:1024
	v_pk_mul_f32 v[12:13], v[70:71], s[12:13] op_sel_hi:[1,0]
	v_pk_mul_f32 v[10:11], v[72:73], s[12:13] op_sel_hi:[1,0]
	v_med3_f32 v18, v12, s52, v175
	v_med3_f32 v13, v13, s52, v175
	v_mov_b32_e32 v12, 0
	v_cvt_pk_fp8_f32 v12, v18, v13
	v_med3_f32 v10, v10, s52, v175
	v_med3_f32 v11, v11, s52, v175
	v_mov_b32_e32 v13, 0
	v_cvt_pk_fp8_f32 v12, v10, v11 op_sel:[0,0,1]
	v_med3_f32 v10, v16, s52, v175
	v_med3_f32 v11, v17, s52, v175
	v_cvt_pk_fp8_f32 v13, v10, v11
	v_med3_f32 v10, v14, s52, v175
	v_med3_f32 v11, v15, s52, v175
	v_pk_mul_f32 v[16:17], v[58:59], s[12:13] op_sel_hi:[1,0]
	v_cvt_pk_fp8_f32 v13, v10, v11 op_sel:[0,0,1]
	v_pk_mul_f32 v[10:11], v[68:69], s[12:13] op_sel_hi:[1,0]
	v_pk_mul_f32 v[14:15], v[60:61], s[12:13] op_sel_hi:[1,0]
	v_med3_f32 v10, v10, s52, v175
	global_store_dwordx2 v[222:223], v[12:13], off offset:1536
	v_pk_mul_f32 v[12:13], v[66:67], s[12:13] op_sel_hi:[1,0]
	v_med3_f32 v11, v11, s52, v175
	v_med3_f32 v18, v12, s52, v175
	v_med3_f32 v13, v13, s52, v175
	v_mov_b32_e32 v12, 0
	v_cvt_pk_fp8_f32 v12, v18, v13
	v_mov_b32_e32 v13, 0
	v_lshl_add_u64 v[8:9], v[6:7], 0, s[22:23]
	v_cvt_pk_fp8_f32 v12, v10, v11 op_sel:[0,0,1]
	v_med3_f32 v10, v16, s52, v175
	v_med3_f32 v11, v17, s52, v175
	v_cvt_pk_fp8_f32 v13, v10, v11
	v_med3_f32 v10, v14, s52, v175
	v_med3_f32 v11, v15, s52, v175
	v_pk_mul_f32 v[16:17], v[46:47], s[12:13] op_sel_hi:[1,0]
	v_cvt_pk_fp8_f32 v13, v10, v11 op_sel:[0,0,1]
	v_add_co_u32_e32 v10, vcc, s65, v6
	v_pk_mul_f32 v[14:15], v[48:49], s[12:13] op_sel_hi:[1,0]
	s_nop 0
	v_addc_co_u32_e32 v11, vcc, 0, v7, vcc
	global_store_dwordx2 v[222:223], v[12:13], off offset:2048
	v_pk_mul_f32 v[12:13], v[54:55], s[12:13] op_sel_hi:[1,0]
	v_pk_mul_f32 v[10:11], v[56:57], s[12:13] op_sel_hi:[1,0]
	v_med3_f32 v18, v12, s52, v175
	v_med3_f32 v13, v13, s52, v175
	v_mov_b32_e32 v12, 0
	v_cvt_pk_fp8_f32 v12, v18, v13
	v_med3_f32 v10, v10, s52, v175
	v_med3_f32 v11, v11, s52, v175
	v_mov_b32_e32 v13, 0
	v_cvt_pk_fp8_f32 v12, v10, v11 op_sel:[0,0,1]
	v_med3_f32 v10, v16, s52, v175
	v_med3_f32 v11, v17, s52, v175
	v_cvt_pk_fp8_f32 v13, v10, v11
	v_med3_f32 v10, v14, s52, v175
	v_med3_f32 v11, v15, s52, v175
	v_pk_mul_f32 v[16:17], v[42:43], s[12:13] op_sel_hi:[1,0]
	v_cvt_pk_fp8_f32 v13, v10, v11 op_sel:[0,0,1]
	v_pk_mul_f32 v[10:11], v[52:53], s[12:13] op_sel_hi:[1,0]
	v_pk_mul_f32 v[14:15], v[44:45], s[12:13] op_sel_hi:[1,0]
	v_med3_f32 v10, v10, s52, v175
	global_store_dwordx2 v[222:223], v[12:13], off offset:2560
	v_pk_mul_f32 v[12:13], v[50:51], s[12:13] op_sel_hi:[1,0]
	v_med3_f32 v11, v11, s52, v175
	v_med3_f32 v18, v12, s52, v175
	v_med3_f32 v13, v13, s52, v175
	v_mov_b32_e32 v12, 0
	v_cvt_pk_fp8_f32 v12, v18, v13
	v_mov_b32_e32 v13, 0
	v_lshl_add_u64 v[8:9], v[6:7], 0, s[40:41]
	v_add_co_u32_e32 v6, vcc, s30, v6
	v_cvt_pk_fp8_f32 v12, v10, v11 op_sel:[0,0,1]
	v_med3_f32 v10, v16, s52, v175
	v_med3_f32 v11, v17, s52, v175
	v_cvt_pk_fp8_f32 v13, v10, v11
	v_med3_f32 v10, v14, s52, v175
	v_med3_f32 v11, v15, s52, v175
	v_addc_co_u32_e32 v7, vcc, 0, v7, vcc
	v_cvt_pk_fp8_f32 v13, v10, v11 op_sel:[0,0,1]
	v_pk_mul_f32 v[10:11], v[38:39], s[12:13] op_sel_hi:[1,0]
	v_pk_mul_f32 v[14:15], v[34:35], s[12:13] op_sel_hi:[1,0]
	v_med3_f32 v16, v10, s52, v175
	v_med3_f32 v11, v11, s52, v175
	v_mov_b32_e32 v10, 0
	v_cvt_pk_fp8_f32 v10, v16, v11
	global_store_dwordx2 v[222:223], v[12:13], off offset:3072
	v_pk_mul_f32 v[6:7], v[40:41], s[12:13] op_sel_hi:[1,0]
	v_mov_b32_e32 v11, 0
	v_med3_f32 v6, v6, s52, v175
	v_med3_f32 v7, v7, s52, v175
	v_cvt_pk_fp8_f32 v10, v6, v7 op_sel:[0,0,1]
	v_med3_f32 v6, v14, s52, v175
	v_med3_f32 v7, v15, s52, v175
	v_cvt_pk_fp8_f32 v11, v6, v7
	v_pk_mul_f32 v[12:13], v[36:37], s[12:13] op_sel_hi:[1,0]
	s_nop 0
	v_med3_f32 v6, v12, s52, v175
	v_med3_f32 v7, v13, s52, v175
	v_cvt_pk_fp8_f32 v11, v6, v7 op_sel:[0,0,1]
	global_store_dwordx2 v[222:223], v[10:11], off offset:3584
	s_cbranch_execnz .LBB0_222

.Lmid1046:
	ds_read_b128 v[136:139], v175
	ds_read_b128 v[140:143], v175 offset:1024
	ds_read_b128 v[144:147], v175 offset:2048
	ds_read_b128 v[148:151], v175 offset:3072
	ds_read_b128 v[152:155], v176
	ds_read_b128 v[156:159], v176 offset:1024
	ds_read_b128 v[160:163], v176 offset:2048
	ds_read_b128 v[178:181], v176 offset:3072
	ds_read_b128 v[182:185], v174 offset:32768
	ds_read_b128 v[186:189], v174 offset:33792
	ds_read_b128 v[190:193], v174 offset:34816
	ds_read_b128 v[194:197], v174 offset:35840
	ds_read_b128 v[198:201], v174 offset:36864
	ds_read_b128 v[202:205], v174 offset:37888
	ds_read_b128 v[206:209], v174 offset:38912
	ds_read_b128 v[210:213], v174 offset:39936
	s_add_u32 s28, s25, 0x40100
	s_addc_u32 s29, s33, 0
	s_mov_b32 s25, m0
	s_mov_b32 m0, s85
	s_nop 2
	global_load_lds_dwordx4 v165, s[28:29]
	s_mov_b32 m0, s25
	s_nop 0
	s_mov_b32 s25, m0
	s_mov_b32 m0, s86
	s_nop 2
	global_load_lds_dwordx4 v167, s[28:29]
	s_mov_b32 m0, s25
	s_waitcnt vmcnt(8)
	s_waitcnt lgkmcnt(0)
	s_barrier
	s_setprio 1
	s_waitcnt lgkmcnt(7)
	v_mfma_f32_16x16x32_bf16 v[26:29], v[136:139], v[182:185], v[26:29]
	v_mfma_f32_16x16x32_bf16 v[30:33], v[144:147], v[182:185], v[30:33]
	s_waitcnt lgkmcnt(5)
	v_mfma_f32_16x16x32_bf16 v[50:53], v[136:139], v[190:193], v[50:53]
	v_mfma_f32_16x16x32_bf16 v[54:57], v[144:147], v[190:193], v[54:57]
	s_waitcnt lgkmcnt(3)
	v_mfma_f32_16x16x32_bf16 v[74:77], v[136:139], v[198:201], v[74:77]
	v_mfma_f32_16x16x32_bf16 v[78:81], v[144:147], v[198:201], v[78:81]
	s_waitcnt lgkmcnt(1)
	v_mfma_f32_16x16x32_bf16 v[94:97], v[136:139], v[206:209], v[94:97]
	v_mfma_f32_16x16x32_bf16 v[102:105], v[144:147], v[206:209], v[102:105]
	v_mfma_f32_16x16x32_bf16 v[26:29], v[140:143], v[186:189], v[26:29]
	v_mfma_f32_16x16x32_bf16 v[30:33], v[148:151], v[186:189], v[30:33]
	v_mfma_f32_16x16x32_bf16 v[50:53], v[140:143], v[194:197], v[50:53]
	v_mfma_f32_16x16x32_bf16 v[54:57], v[148:151], v[194:197], v[54:57]
	v_mfma_f32_16x16x32_bf16 v[74:77], v[140:143], v[202:205], v[74:77]
	v_mfma_f32_16x16x32_bf16 v[78:81], v[148:151], v[202:205], v[78:81]
	s_waitcnt lgkmcnt(0)
	v_mfma_f32_16x16x32_bf16 v[94:97], v[140:143], v[210:213], v[94:97]
	v_mfma_f32_16x16x32_bf16 v[102:105], v[148:151], v[210:213], v[102:105]
	s_setprio 0
	s_setprio 1
	v_mfma_f32_16x16x32_bf16 v[38:41], v[152:155], v[182:185], v[38:41]
	v_mfma_f32_16x16x32_bf16 v[42:45], v[160:163], v[182:185], v[42:45]
	v_mfma_f32_16x16x32_bf16 v[62:65], v[152:155], v[190:193], v[62:65]
	v_mfma_f32_16x16x32_bf16 v[66:69], v[160:163], v[190:193], v[66:69]
	v_mfma_f32_16x16x32_bf16 v[82:85], v[152:155], v[198:201], v[82:85]
	v_mfma_f32_16x16x32_bf16 v[90:93], v[160:163], v[198:201], v[90:93]
	v_mfma_f32_16x16x32_bf16 v[106:109], v[152:155], v[206:209], v[106:109]
	v_mfma_f32_16x16x32_bf16 v[114:117], v[160:163], v[206:209], v[114:117]
	v_mfma_f32_16x16x32_bf16 v[38:41], v[156:159], v[186:189], v[38:41]
	v_mfma_f32_16x16x32_bf16 v[42:45], v[178:181], v[186:189], v[42:45]
	v_mfma_f32_16x16x32_bf16 v[62:65], v[156:159], v[194:197], v[62:65]
	v_mfma_f32_16x16x32_bf16 v[66:69], v[178:181], v[194:197], v[66:69]
	v_mfma_f32_16x16x32_bf16 v[82:85], v[156:159], v[202:205], v[82:85]
	v_mfma_f32_16x16x32_bf16 v[90:93], v[178:181], v[202:205], v[90:93]
	v_mfma_f32_16x16x32_bf16 v[106:109], v[156:159], v[210:213], v[106:109]
	v_mfma_f32_16x16x32_bf16 v[114:117], v[178:181], v[210:213], v[114:117]
	s_setprio 0
	s_barrier
	ds_read_b128 v[182:185], v174 offset:49152
	ds_read_b128 v[186:189], v174 offset:50176
	ds_read_b128 v[190:193], v174 offset:51200
	ds_read_b128 v[194:197], v174 offset:52224
	ds_read_b128 v[198:201], v174 offset:53248
	ds_read_b128 v[202:205], v174 offset:54272
	ds_read_b128 v[206:209], v174 offset:55296
	ds_read_b128 v[210:213], v174 offset:56320
	s_add_u32 s28, s23, 0x180
	s_addc_u32 s29, s24, 0
	s_mov_b32 s25, m0
	s_mov_b32 m0, s92
	s_nop 2
	global_load_lds_dwordx4 v166, s[28:29]
	s_mov_b32 m0, s25
	s_nop 0
	s_mov_b32 s25, m0
	s_mov_b32 m0, s93
	s_nop 2
	global_load_lds_dwordx4 v168, s[28:29]
	s_mov_b32 m0, s25
	s_add_u32 s28, s23, 0x40180
	s_addc_u32 s29, s24, 0
	s_mov_b32 s23, m0
	s_mov_b32 m0, s96
	s_nop 2
	global_load_lds_dwordx4 v166, s[28:29]
	s_mov_b32 m0, s23
	s_nop 0
	s_mov_b32 s23, m0
	s_mov_b32 m0, s97
	s_nop 2
	global_load_lds_dwordx4 v168, s[28:29]
	s_mov_b32 m0, s23
	s_nop 0
	s_mov_b32 s23, m0
	s_mov_b32 m0, s94
	s_nop 2
	global_load_lds_dwordx4 v165, s[58:59]
	s_mov_b32 m0, s23
	s_nop 0
	s_mov_b32 s23, m0
	s_mov_b32 m0, s95
	s_nop 2
	global_load_lds_dwordx4 v167, s[58:59]
	s_mov_b32 m0, s23
	s_waitcnt vmcnt(8)
	s_waitcnt lgkmcnt(0)
	s_barrier
	s_setprio 1
	s_waitcnt lgkmcnt(7)
	v_mfma_f32_16x16x32_bf16 v[118:121], v[136:139], v[182:185], v[118:121]
	v_mfma_f32_16x16x32_bf16 v[126:129], v[144:147], v[182:185], v[126:129]
	s_waitcnt lgkmcnt(5)
	v_mfma_f32_16x16x32_bf16 v[98:101], v[136:139], v[190:193], v[98:101]
	v_mfma_f32_16x16x32_bf16 v[86:89], v[144:147], v[190:193], v[86:89]
	s_waitcnt lgkmcnt(3)
	v_mfma_f32_16x16x32_bf16 v[46:49], v[136:139], v[198:201], v[46:49]
	v_mfma_f32_16x16x32_bf16 v[34:37], v[144:147], v[198:201], v[34:37]
	s_waitcnt lgkmcnt(1)
	v_mfma_f32_16x16x32_bf16 v[14:17], v[136:139], v[206:209], v[14:17]
	v_mfma_f32_16x16x32_bf16 v[10:13], v[144:147], v[206:209], v[10:13]
	v_mfma_f32_16x16x32_bf16 v[118:121], v[140:143], v[186:189], v[118:121]
	v_mfma_f32_16x16x32_bf16 v[126:129], v[148:151], v[186:189], v[126:129]
	v_mfma_f32_16x16x32_bf16 v[98:101], v[140:143], v[194:197], v[98:101]
	v_mfma_f32_16x16x32_bf16 v[86:89], v[148:151], v[194:197], v[86:89]
	v_mfma_f32_16x16x32_bf16 v[46:49], v[140:143], v[202:205], v[46:49]
	v_mfma_f32_16x16x32_bf16 v[34:37], v[148:151], v[202:205], v[34:37]
	s_waitcnt lgkmcnt(0)
	v_mfma_f32_16x16x32_bf16 v[14:17], v[140:143], v[210:213], v[14:17]
	v_mfma_f32_16x16x32_bf16 v[10:13], v[148:151], v[210:213], v[10:13]
	s_setprio 0
	s_setprio 1
	v_mfma_f32_16x16x32_bf16 v[122:125], v[152:155], v[182:185], v[122:125]
	v_mfma_f32_16x16x32_bf16 v[110:113], v[160:163], v[182:185], v[110:113]
	v_mfma_f32_16x16x32_bf16 v[70:73], v[152:155], v[190:193], v[70:73]
	v_mfma_f32_16x16x32_bf16 v[58:61], v[160:163], v[190:193], v[58:61]
	v_mfma_f32_16x16x32_bf16 v[22:25], v[152:155], v[198:201], v[22:25]
	v_mfma_f32_16x16x32_bf16 v[18:21], v[160:163], v[198:201], v[18:21]
	v_mfma_f32_16x16x32_bf16 v[6:9], v[152:155], v[206:209], v[6:9]
	v_mfma_f32_16x16x32_bf16 v[2:5], v[160:163], v[206:209], v[2:5]
	v_mfma_f32_16x16x32_bf16 v[122:125], v[156:159], v[186:189], v[122:125]
	v_mfma_f32_16x16x32_bf16 v[110:113], v[178:181], v[186:189], v[110:113]
	v_mfma_f32_16x16x32_bf16 v[70:73], v[156:159], v[194:197], v[70:73]
	v_mfma_f32_16x16x32_bf16 v[58:61], v[178:181], v[194:197], v[58:61]
	v_mfma_f32_16x16x32_bf16 v[22:25], v[156:159], v[202:205], v[22:25]
	v_mfma_f32_16x16x32_bf16 v[18:21], v[178:181], v[202:205], v[18:21]
	v_mfma_f32_16x16x32_bf16 v[6:9], v[156:159], v[210:213], v[6:9]
	v_mfma_f32_16x16x32_bf16 v[2:5], v[178:181], v[210:213], v[2:5]
	s_setprio 0
	s_barrier
	s_add_i32 s3, s3, 2
	s_add_u32 s56, s56, 0x100
	s_addc_u32 s57, s57, 0
	s_cmp_gt_u32 s3, 5
	s_cbranch_scc0 .LBB0_1046
	s_ashr_i32 s55, s54, 31
	s_lshl_b64 s[24:25], s[54:55], 19
	s_add_u32 s56, s69, s24
	s_addc_u32 s57, s76, s25
	s_ashr_i32 s23, s22, 31
	s_lshl_b64 s[24:25], s[22:23], 19
	s_add_u32 s58, s77, s24
	s_addc_u32 s59, s78, s25
	s_lshl_b32 s3, s60, 18
	s_lshl_b32 s23, s2, 8
	s_lshl_b32 s32, s2, 16
	s_add_i32 s2, s32, s3
	v_lshrrev_b32_e32 v214, 6, v0
	v_lshlrev_b32_e32 v214, 13, v214
	v_and_b32_e32 v215, 63, v0
	v_lshl_add_u32 v214, v215, 3, v214
	v_add_u32_e32 v134, s2, v214
	global_load_dwordx2 v[162:163], v134, s[14:15]
	global_load_dwordx2 v[178:179], v134, s[16:17]
	v_or_b32_e32 v136, 0x200, v134
	v_add_u32_e32 v137, 0x400, v134
	v_add_u32_e32 v138, 0x600, v134
	v_add_u32_e32 v139, 0x800, v134
	v_add_u32_e32 v140, 0xa00, v134
	v_add_u32_e32 v141, 0xc00, v134
	v_add_u32_e32 v161, 0xe00, v134
	global_load_dwordx2 v[180:181], v136, s[14:15]
	global_load_dwordx2 v[182:183], v136, s[16:17]
	global_load_dwordx2 v[158:159], v137, s[14:15]
	global_load_dwordx2 v[156:157], v137, s[16:17]
	global_load_dwordx2 v[154:155], v138, s[14:15]
	global_load_dwordx2 v[152:153], v138, s[16:17]
	global_load_dwordx2 v[150:151], v139, s[14:15]
	global_load_dwordx2 v[148:149], v139, s[16:17]
	global_load_dwordx2 v[146:147], v140, s[14:15]
	global_load_dwordx2 v[144:145], v140, s[16:17]
	global_load_dwordx2 v[142:143], v141, s[14:15]
	s_nop 0
	global_load_dwordx2 v[140:141], v141, s[16:17]
	s_nop 0
	global_load_dwordx2 v[138:139], v161, s[14:15]
	global_load_dwordx2 v[136:137], v161, s[16:17]
	v_add_u32_e32 v160, 0x1000, v134
	s_and_b64 s[2:3], s[4:5], exec
	s_cselect_b32 s2, s57, s65
	s_cselect_b32 s3, s56, s64
	s_cselect_b32 s24, s59, s63
	s_cselect_b32 s25, s58, s62
	s_add_u32 s28, s64, 0x500
	s_addc_u32 s29, s65, 0
	s_add_u32 s30, s62, 0x500
	s_addc_u32 s31, s63, 0
	s_mov_b32 s33, 6
	s_waitcnt vmcnt(15)
	v_cvt_pk_f32_fp8_e32 v[184:185], v162
	s_waitcnt vmcnt(14)
	v_cvt_pk_f32_fp8_e32 v[190:191], v178
	v_cvt_pk_f32_fp8_e32 v[188:189], v163
	v_cvt_pk_f32_fp8_sdwa v[192:193], v178 src0_sel:WORD_1
	v_cvt_pk_f32_fp8_e32 v[194:195], v179
	v_max_f32_e32 v161, v190, v190
	v_max_f32_e32 v190, v191, v191
	v_med3_f32 v161, v161, s35, v177
	v_med3_f32 v184, v184, s35, v177
	v_max_f32_e32 v191, v192, v192
	v_max_f32_e32 v192, v193, v193
	v_max_f32_e32 v193, v194, v194
	v_max_f32_e32 v194, v195, v195
	v_med3_f32 v190, v190, s35, v177
	v_med3_f32 v185, v185, s35, v177
	v_med3_f32 v188, v188, s35, v177
	v_mul_f32_e32 v161, 0xbfb8aa3b, v161
	v_mul_f32_e32 v195, 0xbfb8aa3b, v184
	v_cvt_pk_f32_fp8_sdwa v[186:187], v162 src0_sel:WORD_1
	v_cvt_pk_f32_fp8_sdwa v[162:163], v163 src0_sel:WORD_1
	v_med3_f32 v194, v194, s35, v177
	v_med3_f32 v189, v189, s35, v177
	v_mul_f32_e32 v190, 0xbfb8aa3b, v190
	v_mul_f32_e32 v196, 0xbfb8aa3b, v185
	v_mul_f32_e32 v199, 0xbfb8aa3b, v188
	v_exp_f32_e32 v184, v161
	v_exp_f32_e32 v161, v195
	v_mul_f32_e32 v200, 0xbfb8aa3b, v194
	v_mul_f32_e32 v189, 0xbfb8aa3b, v189
	v_exp_f32_e32 v185, v190
	v_exp_f32_e32 v190, v196
	v_exp_f32_e32 v194, v199
	v_exp_f32_e32 v195, v189
	v_cvt_pk_f32_fp8_sdwa v[178:179], v179 src0_sel:WORD_1
	v_add_f32_e32 v161, 1.0, v161
	v_add_f32_e32 v189, 1.0, v190
	v_rcp_f32_e32 v190, v161
	v_add_f32_e32 v161, 1.0, v194
	v_med3_f32 v162, v162, s35, v177
	v_rcp_f32_e32 v194, v161
	v_add_f32_e32 v161, 1.0, v195
	v_mul_f32_e32 v162, 0xbfb8aa3b, v162
	v_rcp_f32_e32 v195, v161
	v_max_f32_e32 v161, v178, v178
	v_exp_f32_e32 v178, v162
	v_med3_f32 v161, v161, s35, v177
	v_med3_f32 v163, v163, s35, v177
	v_mul_f32_e32 v161, 0xbfb8aa3b, v161
	v_mul_f32_e32 v163, 0xbfb8aa3b, v163
	v_exp_f32_e32 v162, v161
	v_add_f32_e32 v161, 1.0, v178
	v_max_f32_e32 v178, v179, v179
	v_exp_f32_e32 v179, v163
	v_med3_f32 v191, v191, s35, v177
	v_med3_f32 v186, v186, s35, v177
	v_med3_f32 v192, v192, s35, v177
	v_med3_f32 v187, v187, s35, v177
	v_mul_f32_e32 v191, 0xbfb8aa3b, v191
	v_mul_f32_e32 v197, 0xbfb8aa3b, v186
	v_mul_f32_e32 v192, 0xbfb8aa3b, v192
	v_mul_f32_e32 v198, 0xbfb8aa3b, v187
	v_med3_f32 v178, v178, s35, v177
	v_exp_f32_e32 v186, v191
	v_exp_f32_e32 v191, v197
	v_exp_f32_e32 v187, v192
	v_exp_f32_e32 v192, v198
	v_mul_f32_e32 v163, 0xbfb8aa3b, v178
	v_exp_f32_e32 v163, v163
	v_rcp_f32_e32 v178, v161
	v_add_f32_e32 v161, 1.0, v179
	v_med3_f32 v193, v193, s35, v177
	v_rcp_f32_e32 v179, v161
	v_mul_f32_e32 v193, 0xbfb8aa3b, v193
	v_exp_f32_e32 v188, v193
	v_add_f32_e32 v193, 1.0, v191
	v_add_f32_e32 v196, 1.0, v192
	v_rcp_f32_e32 v192, v193
	v_rcp_f32_e32 v193, v196
	v_pk_add_f32 v[162:163], v[162:163], 1.0 op_sel_hi:[1,0]
	v_pk_add_f32 v[186:187], v[186:187], 1.0 op_sel_hi:[1,0]
	v_pk_mul_f32 v[162:163], v[178:179], v[162:163]
	v_pk_mul_f32 v[186:187], v[192:193], v[186:187]
	v_pk_mul_f32 v[32:33], v[32:33], v[162:163]
	s_waitcnt vmcnt(13)
	v_cvt_pk_f32_fp8_e32 v[162:163], v180
	v_pk_mul_f32 v[28:29], v[28:29], v[186:187]
	s_waitcnt vmcnt(12)
	v_cvt_pk_f32_fp8_e32 v[186:187], v182
	v_rcp_f32_e32 v191, v189
	v_med3_f32 v162, v162, s35, v177
	v_mul_f32_e32 v162, 0xbfb8aa3b, v162
	v_max_f32_e32 v161, v186, v186
	v_exp_f32_e32 v186, v162
	v_exp_f32_e32 v189, v200
	v_med3_f32 v161, v161, s35, v177
	v_cvt_pk_f32_fp8_sdwa v[178:179], v180 src0_sel:WORD_1
	v_mul_f32_e32 v161, 0xbfb8aa3b, v161
	v_med3_f32 v163, v163, s35, v177
	v_pk_add_f32 v[184:185], v[184:185], 1.0 op_sel_hi:[1,0]
	v_exp_f32_e32 v162, v161
	v_add_f32_e32 v161, 1.0, v186
	v_mul_f32_e32 v163, 0xbfb8aa3b, v163
	v_pk_mul_f32 v[184:185], v[190:191], v[184:185]
	v_rcp_f32_e32 v186, v161
	v_max_f32_e32 v161, v187, v187
	v_exp_f32_e32 v187, v163
	v_pk_mul_f32 v[26:27], v[26:27], v[184:185]
	v_pk_add_f32 v[184:185], v[188:189], 1.0 op_sel_hi:[1,0]
	v_cvt_pk_f32_fp8_sdwa v[188:189], v182 src0_sel:WORD_1
	v_med3_f32 v161, v161, s35, v177
	v_mul_f32_e32 v161, 0xbfb8aa3b, v161
	v_med3_f32 v178, v178, s35, v177
	v_exp_f32_e32 v163, v161
	v_add_f32_e32 v161, 1.0, v187
	v_mul_f32_e32 v178, 0xbfb8aa3b, v178
	v_pk_mul_f32 v[184:185], v[194:195], v[184:185]
	v_rcp_f32_e32 v187, v161
	v_max_f32_e32 v161, v188, v188
	v_exp_f32_e32 v188, v178
	v_pk_mul_f32 v[30:31], v[30:31], v[184:185]
	v_cvt_pk_f32_fp8_e32 v[184:185], v181
	v_med3_f32 v161, v161, s35, v177
	v_med3_f32 v179, v179, s35, v177
	v_mul_f32_e32 v161, 0xbfb8aa3b, v161
	v_mul_f32_e32 v179, 0xbfb8aa3b, v179
	v_pk_add_f32 v[162:163], v[162:163], 1.0 op_sel_hi:[1,0]
	v_exp_f32_e32 v178, v161
	v_add_f32_e32 v161, 1.0, v188
	v_max_f32_e32 v188, v189, v189
	v_exp_f32_e32 v189, v179
	v_pk_mul_f32 v[162:163], v[186:187], v[162:163]
	v_cvt_pk_f32_fp8_e32 v[190:191], v183
	v_pk_mul_f32 v[38:39], v[38:39], v[162:163]
	v_med3_f32 v162, v184, s35, v177
	v_med3_f32 v188, v188, s35, v177
	v_mul_f32_e32 v162, 0xbfb8aa3b, v162
	v_mul_f32_e32 v179, 0xbfb8aa3b, v188
	v_rcp_f32_e32 v188, v161
	v_add_f32_e32 v161, 1.0, v189
	v_exp_f32_e32 v163, v162
	v_exp_f32_e32 v179, v179
	v_rcp_f32_e32 v189, v161
	v_med3_f32 v161, v190, s35, v177
	v_mul_f32_e32 v161, 0xbfb8aa3b, v161
	v_exp_f32_e32 v162, v161
	v_add_f32_e32 v161, 1.0, v163
	v_cvt_pk_f32_fp8_sdwa v[180:181], v181 src0_sel:WORD_1
	v_pk_add_f32 v[178:179], v[178:179], 1.0 op_sel_hi:[1,0]
	v_med3_f32 v163, v185, s35, v177
	v_pk_mul_f32 v[178:179], v[188:189], v[178:179]
	v_mul_f32_e32 v163, 0xbfb8aa3b, v163
	v_pk_mul_f32 v[40:41], v[40:41], v[178:179]
	v_exp_f32_e32 v179, v163
	v_cvt_pk_f32_fp8_sdwa v[182:183], v183 src0_sel:WORD_1
	v_rcp_f32_e32 v178, v161
	v_med3_f32 v161, v191, s35, v177
	v_mul_f32_e32 v161, 0xbfb8aa3b, v161
	v_med3_f32 v180, v180, s35, v177
	v_exp_f32_e32 v163, v161
	v_add_f32_e32 v161, 1.0, v179
	v_mul_f32_e32 v180, 0xbfb8aa3b, v180
	v_rcp_f32_e32 v179, v161
	v_max_f32_e32 v161, v182, v182
	v_exp_f32_e32 v182, v180
	v_med3_f32 v161, v161, s35, v177
	v_med3_f32 v181, v181, s35, v177
	v_mul_f32_e32 v161, 0xbfb8aa3b, v161
	v_mul_f32_e32 v181, 0xbfb8aa3b, v181
	v_exp_f32_e32 v180, v161
	v_add_f32_e32 v161, 1.0, v182
	v_max_f32_e32 v182, v183, v183
	v_exp_f32_e32 v183, v181
	v_med3_f32 v182, v182, s35, v177
	v_mul_f32_e32 v181, 0xbfb8aa3b, v182
	v_exp_f32_e32 v181, v181
	v_rcp_f32_e32 v182, v161
	v_add_f32_e32 v161, 1.0, v183
	v_pk_add_f32 v[162:163], v[162:163], 1.0 op_sel_hi:[1,0]
	v_rcp_f32_e32 v183, v161
	v_pk_mul_f32 v[162:163], v[178:179], v[162:163]
	v_pk_add_f32 v[180:181], v[180:181], 1.0 op_sel_hi:[1,0]
	v_pk_mul_f32 v[42:43], v[42:43], v[162:163]
	s_waitcnt vmcnt(11)
	v_cvt_pk_f32_fp8_e32 v[162:163], v158
	v_pk_mul_f32 v[178:179], v[182:183], v[180:181]
	s_waitcnt vmcnt(10)
	v_cvt_pk_f32_fp8_e32 v[182:183], v156
	v_pk_mul_f32 v[44:45], v[44:45], v[178:179]
	v_med3_f32 v162, v162, s35, v177
	v_mul_f32_e32 v162, 0xbfb8aa3b, v162
	v_max_f32_e32 v161, v182, v182
	v_exp_f32_e32 v182, v162
	v_med3_f32 v161, v161, s35, v177
	v_cvt_pk_f32_fp8_sdwa v[178:179], v158 src0_sel:WORD_1
	v_mul_f32_e32 v161, 0xbfb8aa3b, v161
	v_med3_f32 v163, v163, s35, v177
	v_exp_f32_e32 v162, v161
	v_add_f32_e32 v161, 1.0, v182
	v_mul_f32_e32 v163, 0xbfb8aa3b, v163
	v_rcp_f32_e32 v182, v161
	v_max_f32_e32 v161, v183, v183
	v_exp_f32_e32 v183, v163
	v_cvt_pk_f32_fp8_sdwa v[184:185], v156 src0_sel:WORD_1
	v_med3_f32 v161, v161, s35, v177
	v_mul_f32_e32 v161, 0xbfb8aa3b, v161
	v_med3_f32 v178, v178, s35, v177
	v_exp_f32_e32 v163, v161
	v_add_f32_e32 v161, 1.0, v183
	v_mul_f32_e32 v178, 0xbfb8aa3b, v178
	v_rcp_f32_e32 v183, v161
	v_max_f32_e32 v161, v184, v184
	v_exp_f32_e32 v184, v178
	v_cvt_pk_f32_fp8_e32 v[180:181], v159
	v_med3_f32 v161, v161, s35, v177
	v_med3_f32 v179, v179, s35, v177
	v_mul_f32_e32 v161, 0xbfb8aa3b, v161
	v_mul_f32_e32 v179, 0xbfb8aa3b, v179
	v_pk_add_f32 v[162:163], v[162:163], 1.0 op_sel_hi:[1,0]
	v_cvt_pk_f32_fp8_sdwa v[158:159], v159 src0_sel:WORD_1
	v_exp_f32_e32 v178, v161
	v_add_f32_e32 v161, 1.0, v184
	v_max_f32_e32 v184, v185, v185
	v_exp_f32_e32 v185, v179
	v_pk_mul_f32 v[162:163], v[182:183], v[162:163]
	v_cvt_pk_f32_fp8_e32 v[186:187], v157
	v_pk_mul_f32 v[50:51], v[50:51], v[162:163]
	v_med3_f32 v162, v180, s35, v177
	v_med3_f32 v184, v184, s35, v177
	v_mul_f32_e32 v162, 0xbfb8aa3b, v162
	v_cvt_pk_f32_fp8_sdwa v[156:157], v157 src0_sel:WORD_1
	v_mul_f32_e32 v179, 0xbfb8aa3b, v184
	v_rcp_f32_e32 v184, v161
	v_add_f32_e32 v161, 1.0, v185
	v_exp_f32_e32 v163, v162
	v_exp_f32_e32 v179, v179
	v_rcp_f32_e32 v185, v161
	v_med3_f32 v158, v158, s35, v177
	v_med3_f32 v159, v159, s35, v177
	v_med3_f32 v161, v186, s35, v177
	v_mul_f32_e32 v158, 0xbfb8aa3b, v158
	v_mul_f32_e32 v159, 0xbfb8aa3b, v159
	v_mul_f32_e32 v161, 0xbfb8aa3b, v161
	v_exp_f32_e32 v158, v158
	v_exp_f32_e32 v159, v159
	v_exp_f32_e32 v162, v161
	v_add_f32_e32 v161, 1.0, v163
	v_pk_add_f32 v[178:179], v[178:179], 1.0 op_sel_hi:[1,0]
	v_med3_f32 v163, v181, s35, v177
	v_med3_f32 v156, v156, s35, v177
	v_med3_f32 v157, v157, s35, v177
	v_pk_mul_f32 v[178:179], v[184:185], v[178:179]
	v_mul_f32_e32 v163, 0xbfb8aa3b, v163
	v_mul_f32_e32 v156, 0xbfb8aa3b, v156
	v_mul_f32_e32 v157, 0xbfb8aa3b, v157
	v_pk_mul_f32 v[52:53], v[52:53], v[178:179]
	v_exp_f32_e32 v179, v163
	v_exp_f32_e32 v156, v156
	v_add_f32_e32 v158, 1.0, v158
	v_exp_f32_e32 v157, v157
	v_add_f32_e32 v159, 1.0, v159
	v_rcp_f32_e32 v178, v161
	v_rcp_f32_e32 v158, v158
	v_rcp_f32_e32 v159, v159
	v_med3_f32 v161, v187, s35, v177
	v_mul_f32_e32 v161, 0xbfb8aa3b, v161
	v_exp_f32_e32 v163, v161
	v_add_f32_e32 v161, 1.0, v179
	v_pk_add_f32 v[156:157], v[156:157], 1.0 op_sel_hi:[1,0]
	v_rcp_f32_e32 v179, v161
	v_pk_mul_f32 v[156:157], v[158:159], v[156:157]
	v_pk_add_f32 v[162:163], v[162:163], 1.0 op_sel_hi:[1,0]
	v_pk_mul_f32 v[56:57], v[56:57], v[156:157]
	s_waitcnt vmcnt(9)
	v_cvt_pk_f32_fp8_e32 v[156:157], v154
	v_pk_mul_f32 v[162:163], v[178:179], v[162:163]
	s_waitcnt vmcnt(8)
	v_cvt_pk_f32_fp8_e32 v[178:179], v152
	v_cvt_pk_f32_fp8_sdwa v[158:159], v154 src0_sel:WORD_1
	v_med3_f32 v156, v156, s35, v177
	v_mul_f32_e32 v156, 0xbfb8aa3b, v156
	v_max_f32_e32 v161, v178, v178
	v_exp_f32_e32 v178, v156
	v_med3_f32 v157, v157, s35, v177
	v_med3_f32 v156, v161, s35, v177
	v_add_f32_e32 v161, 1.0, v178
	v_mul_f32_e32 v157, 0xbfb8aa3b, v157
	v_rcp_f32_e32 v178, v161
	v_max_f32_e32 v161, v179, v179
	v_exp_f32_e32 v179, v157
	v_cvt_pk_f32_fp8_sdwa v[180:181], v152 src0_sel:WORD_1
	v_med3_f32 v158, v158, s35, v177
	v_med3_f32 v157, v161, s35, v177
	v_add_f32_e32 v161, 1.0, v179
	v_mul_f32_e32 v158, 0xbfb8aa3b, v158
	v_rcp_f32_e32 v179, v161
	v_max_f32_e32 v161, v180, v180
	v_exp_f32_e32 v180, v158
	v_med3_f32 v159, v159, s35, v177
	v_pk_mul_f32 v[54:55], v[54:55], v[162:163]
	v_cvt_pk_f32_fp8_e32 v[162:163], v155
	v_cvt_pk_f32_fp8_sdwa v[154:155], v155 src0_sel:WORD_1
	v_mul_f32_e32 v156, 0xbfb8aa3b, v156
	v_mul_f32_e32 v157, 0xbfb8aa3b, v157
	v_mul_f32_e32 v159, 0xbfb8aa3b, v159
	v_exp_f32_e32 v156, v156
	v_exp_f32_e32 v157, v157
	v_med3_f32 v158, v161, s35, v177
	v_add_f32_e32 v161, 1.0, v180
	v_max_f32_e32 v180, v181, v181
	v_exp_f32_e32 v181, v159
	v_med3_f32 v180, v180, s35, v177
	v_cvt_pk_f32_fp8_e32 v[182:183], v153
	v_cvt_pk_f32_fp8_sdwa v[152:153], v153 src0_sel:WORD_1
	v_mul_f32_e32 v158, 0xbfb8aa3b, v158
	v_mul_f32_e32 v159, 0xbfb8aa3b, v180
	v_exp_f32_e32 v158, v158
	v_exp_f32_e32 v159, v159
	v_rcp_f32_e32 v180, v161
	v_add_f32_e32 v161, 1.0, v181
	v_pk_add_f32 v[156:157], v[156:157], 1.0 op_sel_hi:[1,0]
	v_med3_f32 v154, v154, s35, v177
	v_med3_f32 v155, v155, s35, v177
	v_rcp_f32_e32 v181, v161
	v_pk_mul_f32 v[156:157], v[178:179], v[156:157]
	v_mul_f32_e32 v154, 0xbfb8aa3b, v154
	v_mul_f32_e32 v155, 0xbfb8aa3b, v155
	v_pk_mul_f32 v[62:63], v[62:63], v[156:157]
	v_exp_f32_e32 v154, v154
	v_exp_f32_e32 v155, v155
	v_med3_f32 v157, v162, s35, v177
	v_pk_add_f32 v[158:159], v[158:159], 1.0 op_sel_hi:[1,0]
	v_mul_f32_e32 v157, 0xbfb8aa3b, v157
	v_med3_f32 v152, v152, s35, v177
	v_med3_f32 v153, v153, s35, v177
	v_pk_mul_f32 v[158:159], v[180:181], v[158:159]
	v_exp_f32_e32 v157, v157
	v_mul_f32_e32 v152, 0xbfb8aa3b, v152
	v_mul_f32_e32 v153, 0xbfb8aa3b, v153
	v_pk_mul_f32 v[64:65], v[64:65], v[158:159]
	v_exp_f32_e32 v152, v152
	v_add_f32_e32 v154, 1.0, v154
	v_exp_f32_e32 v153, v153
	v_add_f32_e32 v155, 1.0, v155
	v_med3_f32 v159, v163, s35, v177
	v_rcp_f32_e32 v154, v154
	v_rcp_f32_e32 v155, v155
	v_mul_f32_e32 v159, 0xbfb8aa3b, v159
	v_add_f32_e32 v157, 1.0, v157
	v_exp_f32_e32 v159, v159
	v_rcp_f32_e32 v158, v157
	v_pk_add_f32 v[152:153], v[152:153], 1.0 op_sel_hi:[1,0]
	v_med3_f32 v156, v182, s35, v177
	v_med3_f32 v157, v183, s35, v177
	v_pk_mul_f32 v[152:153], v[154:155], v[152:153]
	v_mul_f32_e32 v156, 0xbfb8aa3b, v156
	v_mul_f32_e32 v157, 0xbfb8aa3b, v157
	v_pk_mul_f32 v[68:69], v[68:69], v[152:153]
	s_waitcnt vmcnt(7)
	v_cvt_pk_f32_fp8_e32 v[152:153], v150
	v_exp_f32_e32 v156, v156
	v_exp_f32_e32 v157, v157
	v_add_f32_e32 v159, 1.0, v159
	v_rcp_f32_e32 v159, v159
	v_pk_add_f32 v[156:157], v[156:157], 1.0 op_sel_hi:[1,0]
	v_med3_f32 v152, v152, s35, v177
	v_pk_mul_f32 v[156:157], v[158:159], v[156:157]
	s_waitcnt vmcnt(6)
	v_cvt_pk_f32_fp8_e32 v[158:159], v148
	v_mul_f32_e32 v152, 0xbfb8aa3b, v152
	v_exp_f32_e32 v161, v152
	v_cvt_pk_f32_fp8_sdwa v[154:155], v150 src0_sel:WORD_1
	v_med3_f32 v153, v153, s35, v177
	v_mul_f32_e32 v153, 0xbfb8aa3b, v153
	v_cvt_pk_f32_fp8_sdwa v[162:163], v148 src0_sel:WORD_1
	v_med3_f32 v152, v158, s35, v177
	v_add_f32_e32 v158, 1.0, v161
	v_exp_f32_e32 v161, v153
	v_med3_f32 v154, v154, s35, v177
	v_mul_f32_e32 v154, 0xbfb8aa3b, v154
	v_med3_f32 v153, v159, s35, v177
	v_add_f32_e32 v159, 1.0, v161
	v_max_f32_e32 v161, v162, v162
	v_exp_f32_e32 v162, v154
	v_med3_f32 v155, v155, s35, v177
	v_pk_mul_f32 v[66:67], v[66:67], v[156:157]
	v_cvt_pk_f32_fp8_e32 v[156:157], v151
	v_cvt_pk_f32_fp8_sdwa v[150:151], v151 src0_sel:WORD_1
	v_mul_f32_e32 v152, 0xbfb8aa3b, v152
	v_mul_f32_e32 v153, 0xbfb8aa3b, v153
	v_mul_f32_e32 v155, 0xbfb8aa3b, v155
	v_exp_f32_e32 v152, v152
	v_exp_f32_e32 v153, v153
	v_med3_f32 v154, v161, s35, v177
	v_add_f32_e32 v161, 1.0, v162
	v_max_f32_e32 v162, v163, v163
	v_exp_f32_e32 v163, v155
	v_rcp_f32_e32 v158, v158
	v_rcp_f32_e32 v159, v159
	v_med3_f32 v162, v162, s35, v177
	v_cvt_pk_f32_fp8_e32 v[178:179], v149
	v_cvt_pk_f32_fp8_sdwa v[148:149], v149 src0_sel:WORD_1
	v_mul_f32_e32 v154, 0xbfb8aa3b, v154
	v_mul_f32_e32 v155, 0xbfb8aa3b, v162
	v_exp_f32_e32 v154, v154
	v_exp_f32_e32 v155, v155
	v_rcp_f32_e32 v162, v161
	v_add_f32_e32 v161, 1.0, v163
	v_pk_add_f32 v[152:153], v[152:153], 1.0 op_sel_hi:[1,0]
	v_med3_f32 v150, v150, s35, v177
	v_med3_f32 v151, v151, s35, v177
	v_rcp_f32_e32 v163, v161
	v_pk_mul_f32 v[152:153], v[158:159], v[152:153]
	v_mul_f32_e32 v150, 0xbfb8aa3b, v150
	v_mul_f32_e32 v151, 0xbfb8aa3b, v151
	v_pk_mul_f32 v[74:75], v[74:75], v[152:153]
	v_exp_f32_e32 v150, v150
	v_exp_f32_e32 v151, v151
	v_med3_f32 v153, v156, s35, v177
	v_pk_add_f32 v[154:155], v[154:155], 1.0 op_sel_hi:[1,0]
	v_mul_f32_e32 v153, 0xbfb8aa3b, v153
	v_med3_f32 v148, v148, s35, v177
	v_med3_f32 v149, v149, s35, v177
	v_pk_mul_f32 v[154:155], v[162:163], v[154:155]
	v_exp_f32_e32 v153, v153
	v_mul_f32_e32 v148, 0xbfb8aa3b, v148
	v_mul_f32_e32 v149, 0xbfb8aa3b, v149
	v_pk_mul_f32 v[76:77], v[76:77], v[154:155]
	v_exp_f32_e32 v148, v148
	v_add_f32_e32 v150, 1.0, v150
	v_exp_f32_e32 v149, v149
	v_add_f32_e32 v151, 1.0, v151
	v_med3_f32 v155, v157, s35, v177
	v_rcp_f32_e32 v150, v150
	v_rcp_f32_e32 v151, v151
	v_mul_f32_e32 v155, 0xbfb8aa3b, v155
	v_add_f32_e32 v153, 1.0, v153
	v_exp_f32_e32 v155, v155
	v_rcp_f32_e32 v154, v153
	v_pk_add_f32 v[148:149], v[148:149], 1.0 op_sel_hi:[1,0]
	v_med3_f32 v152, v178, s35, v177
	v_med3_f32 v153, v179, s35, v177
	v_pk_mul_f32 v[148:149], v[150:151], v[148:149]
	v_mul_f32_e32 v152, 0xbfb8aa3b, v152
	v_mul_f32_e32 v153, 0xbfb8aa3b, v153
	v_pk_mul_f32 v[80:81], v[80:81], v[148:149]
	s_waitcnt vmcnt(5)
	v_cvt_pk_f32_fp8_e32 v[148:149], v146
	v_exp_f32_e32 v152, v152
	v_exp_f32_e32 v153, v153
	v_add_f32_e32 v155, 1.0, v155
	v_rcp_f32_e32 v155, v155
	v_pk_add_f32 v[152:153], v[152:153], 1.0 op_sel_hi:[1,0]
	v_med3_f32 v148, v148, s35, v177
	v_pk_mul_f32 v[152:153], v[154:155], v[152:153]
	s_waitcnt vmcnt(4)
	v_cvt_pk_f32_fp8_e32 v[154:155], v144
	v_mul_f32_e32 v148, 0xbfb8aa3b, v148
	v_exp_f32_e32 v161, v148
	v_cvt_pk_f32_fp8_sdwa v[150:151], v146 src0_sel:WORD_1
	v_med3_f32 v149, v149, s35, v177
	v_mul_f32_e32 v149, 0xbfb8aa3b, v149
	v_med3_f32 v148, v154, s35, v177
	v_add_f32_e32 v154, 1.0, v161
	v_exp_f32_e32 v161, v149
	v_med3_f32 v150, v150, s35, v177
	v_cvt_pk_f32_fp8_sdwa v[156:157], v144 src0_sel:WORD_1
	v_mul_f32_e32 v150, 0xbfb8aa3b, v150
	v_med3_f32 v149, v155, s35, v177
	v_add_f32_e32 v155, 1.0, v161
	v_exp_f32_e32 v161, v150
	v_med3_f32 v151, v151, s35, v177
	v_pk_mul_f32 v[78:79], v[78:79], v[152:153]
	v_cvt_pk_f32_fp8_e32 v[152:153], v147
	v_cvt_pk_f32_fp8_sdwa v[146:147], v147 src0_sel:WORD_1
	v_mul_f32_e32 v148, 0xbfb8aa3b, v148
	v_mul_f32_e32 v149, 0xbfb8aa3b, v149
	v_mul_f32_e32 v151, 0xbfb8aa3b, v151
	v_exp_f32_e32 v148, v148
	v_exp_f32_e32 v149, v149
	v_med3_f32 v150, v156, s35, v177
	v_add_f32_e32 v156, 1.0, v161
	v_exp_f32_e32 v161, v151
	v_rcp_f32_e32 v154, v154
	v_rcp_f32_e32 v155, v155
	v_med3_f32 v157, v157, s35, v177
	v_cvt_pk_f32_fp8_e32 v[158:159], v145
	v_cvt_pk_f32_fp8_sdwa v[144:145], v145 src0_sel:WORD_1
	v_mul_f32_e32 v150, 0xbfb8aa3b, v150
	v_mul_f32_e32 v151, 0xbfb8aa3b, v157
	v_exp_f32_e32 v150, v150
	v_exp_f32_e32 v151, v151
	v_add_f32_e32 v157, 1.0, v161
	v_pk_add_f32 v[148:149], v[148:149], 1.0 op_sel_hi:[1,0]
	v_med3_f32 v146, v146, s35, v177
	v_med3_f32 v147, v147, s35, v177
	v_rcp_f32_e32 v156, v156
	v_rcp_f32_e32 v157, v157
	v_pk_mul_f32 v[148:149], v[154:155], v[148:149]
	v_mul_f32_e32 v146, 0xbfb8aa3b, v146
	v_mul_f32_e32 v147, 0xbfb8aa3b, v147
	v_pk_mul_f32 v[82:83], v[82:83], v[148:149]
	v_exp_f32_e32 v146, v146
	v_exp_f32_e32 v147, v147
	v_med3_f32 v149, v152, s35, v177
	v_pk_add_f32 v[150:151], v[150:151], 1.0 op_sel_hi:[1,0]
	v_mul_f32_e32 v149, 0xbfb8aa3b, v149
	v_med3_f32 v144, v144, s35, v177
	v_med3_f32 v145, v145, s35, v177
	v_pk_mul_f32 v[150:151], v[156:157], v[150:151]
	v_exp_f32_e32 v149, v149
	v_mul_f32_e32 v144, 0xbfb8aa3b, v144
	v_mul_f32_e32 v145, 0xbfb8aa3b, v145
	v_pk_mul_f32 v[84:85], v[84:85], v[150:151]
	v_exp_f32_e32 v144, v144
	v_add_f32_e32 v146, 1.0, v146
	v_exp_f32_e32 v145, v145
	v_add_f32_e32 v147, 1.0, v147
	v_med3_f32 v151, v153, s35, v177
	v_rcp_f32_e32 v146, v146
	v_rcp_f32_e32 v147, v147
	v_mul_f32_e32 v151, 0xbfb8aa3b, v151
	v_add_f32_e32 v149, 1.0, v149
	v_exp_f32_e32 v151, v151
	v_rcp_f32_e32 v150, v149
	v_pk_add_f32 v[144:145], v[144:145], 1.0 op_sel_hi:[1,0]
	v_med3_f32 v148, v158, s35, v177
	v_med3_f32 v149, v159, s35, v177
	v_pk_mul_f32 v[144:145], v[146:147], v[144:145]
	v_mul_f32_e32 v148, 0xbfb8aa3b, v148
	v_mul_f32_e32 v149, 0xbfb8aa3b, v149
	v_pk_mul_f32 v[92:93], v[92:93], v[144:145]
	s_waitcnt vmcnt(3)
	v_cvt_pk_f32_fp8_e32 v[144:145], v142
	v_exp_f32_e32 v148, v148
	v_exp_f32_e32 v149, v149
	v_add_f32_e32 v151, 1.0, v151
	v_rcp_f32_e32 v151, v151
	v_pk_add_f32 v[148:149], v[148:149], 1.0 op_sel_hi:[1,0]
	v_med3_f32 v144, v144, s35, v177
	v_pk_mul_f32 v[148:149], v[150:151], v[148:149]
	s_waitcnt vmcnt(2)
	v_cvt_pk_f32_fp8_e32 v[150:151], v140
	v_mul_f32_e32 v144, 0xbfb8aa3b, v144
	v_exp_f32_e32 v156, v144
	v_cvt_pk_f32_fp8_sdwa v[146:147], v142 src0_sel:WORD_1
	v_med3_f32 v145, v145, s35, v177
	v_mul_f32_e32 v145, 0xbfb8aa3b, v145
	v_med3_f32 v144, v150, s35, v177
	v_add_f32_e32 v150, 1.0, v156
	v_exp_f32_e32 v156, v145
	v_med3_f32 v146, v146, s35, v177
	v_cvt_pk_f32_fp8_sdwa v[152:153], v140 src0_sel:WORD_1
	v_mul_f32_e32 v146, 0xbfb8aa3b, v146
	v_med3_f32 v145, v151, s35, v177
	v_add_f32_e32 v151, 1.0, v156
	v_exp_f32_e32 v156, v146
	v_med3_f32 v147, v147, s35, v177
	v_pk_mul_f32 v[90:91], v[90:91], v[148:149]
	v_cvt_pk_f32_fp8_e32 v[148:149], v143
	v_cvt_pk_f32_fp8_sdwa v[142:143], v143 src0_sel:WORD_1
	v_mul_f32_e32 v144, 0xbfb8aa3b, v144
	v_mul_f32_e32 v145, 0xbfb8aa3b, v145
	v_mul_f32_e32 v147, 0xbfb8aa3b, v147
	v_exp_f32_e32 v144, v144
	v_exp_f32_e32 v145, v145
	v_med3_f32 v146, v152, s35, v177
	v_add_f32_e32 v152, 1.0, v156
	v_exp_f32_e32 v156, v147
	v_rcp_f32_e32 v150, v150
	v_rcp_f32_e32 v151, v151
	v_med3_f32 v153, v153, s35, v177
	v_cvt_pk_f32_fp8_e32 v[154:155], v141
	v_cvt_pk_f32_fp8_sdwa v[140:141], v141 src0_sel:WORD_1
	v_mul_f32_e32 v146, 0xbfb8aa3b, v146
	v_mul_f32_e32 v147, 0xbfb8aa3b, v153
	v_exp_f32_e32 v146, v146
	v_exp_f32_e32 v147, v147
	v_add_f32_e32 v153, 1.0, v156
	v_pk_add_f32 v[144:145], v[144:145], 1.0 op_sel_hi:[1,0]
	v_med3_f32 v142, v142, s35, v177
	v_med3_f32 v143, v143, s35, v177
	v_rcp_f32_e32 v152, v152
	v_rcp_f32_e32 v153, v153
	v_pk_mul_f32 v[144:145], v[150:151], v[144:145]
	v_mul_f32_e32 v142, 0xbfb8aa3b, v142
	v_mul_f32_e32 v143, 0xbfb8aa3b, v143
	v_pk_mul_f32 v[94:95], v[94:95], v[144:145]
	v_exp_f32_e32 v142, v142
	v_exp_f32_e32 v143, v143
	v_med3_f32 v145, v148, s35, v177
	v_pk_add_f32 v[146:147], v[146:147], 1.0 op_sel_hi:[1,0]
	v_mul_f32_e32 v145, 0xbfb8aa3b, v145
	v_med3_f32 v140, v140, s35, v177
	v_med3_f32 v141, v141, s35, v177
	v_pk_mul_f32 v[146:147], v[152:153], v[146:147]
	v_exp_f32_e32 v145, v145
	v_mul_f32_e32 v140, 0xbfb8aa3b, v140
	v_mul_f32_e32 v141, 0xbfb8aa3b, v141
	v_pk_mul_f32 v[96:97], v[96:97], v[146:147]
	v_exp_f32_e32 v140, v140
	v_add_f32_e32 v142, 1.0, v142
	v_exp_f32_e32 v141, v141
	v_add_f32_e32 v143, 1.0, v143
	v_med3_f32 v147, v149, s35, v177
	v_rcp_f32_e32 v142, v142
	v_rcp_f32_e32 v143, v143
	v_mul_f32_e32 v147, 0xbfb8aa3b, v147
	v_add_f32_e32 v145, 1.0, v145
	v_exp_f32_e32 v147, v147
	v_rcp_f32_e32 v146, v145
	v_pk_add_f32 v[140:141], v[140:141], 1.0 op_sel_hi:[1,0]
	v_med3_f32 v144, v154, s35, v177
	v_med3_f32 v145, v155, s35, v177
	v_pk_mul_f32 v[140:141], v[142:143], v[140:141]
	v_mul_f32_e32 v144, 0xbfb8aa3b, v144
	v_mul_f32_e32 v145, 0xbfb8aa3b, v145
	v_pk_mul_f32 v[104:105], v[104:105], v[140:141]
	s_waitcnt vmcnt(1)
	v_cvt_pk_f32_fp8_e32 v[140:141], v138
	v_exp_f32_e32 v144, v144
	v_exp_f32_e32 v145, v145
	v_add_f32_e32 v147, 1.0, v147
	v_rcp_f32_e32 v147, v147
	v_pk_add_f32 v[144:145], v[144:145], 1.0 op_sel_hi:[1,0]
	v_med3_f32 v140, v140, s35, v177
	v_pk_mul_f32 v[144:145], v[146:147], v[144:145]
	s_waitcnt vmcnt(0)
	v_cvt_pk_f32_fp8_e32 v[146:147], v136
	v_mul_f32_e32 v140, 0xbfb8aa3b, v140
	v_exp_f32_e32 v152, v140
	v_cvt_pk_f32_fp8_sdwa v[142:143], v138 src0_sel:WORD_1
	v_med3_f32 v141, v141, s35, v177
	v_mul_f32_e32 v141, 0xbfb8aa3b, v141
	v_med3_f32 v140, v146, s35, v177
	v_add_f32_e32 v146, 1.0, v152
	v_exp_f32_e32 v152, v141
	v_med3_f32 v142, v142, s35, v177
	v_cvt_pk_f32_fp8_sdwa v[148:149], v136 src0_sel:WORD_1
	v_mul_f32_e32 v142, 0xbfb8aa3b, v142
	v_med3_f32 v141, v147, s35, v177
	v_add_f32_e32 v147, 1.0, v152
	v_exp_f32_e32 v152, v142
	v_med3_f32 v143, v143, s35, v177
	v_mul_f32_e32 v140, 0xbfb8aa3b, v140
	v_mul_f32_e32 v141, 0xbfb8aa3b, v141
	v_mul_f32_e32 v143, 0xbfb8aa3b, v143
	v_exp_f32_e32 v140, v140
	v_exp_f32_e32 v141, v141
	v_med3_f32 v142, v148, s35, v177
	v_add_f32_e32 v148, 1.0, v152
	v_exp_f32_e32 v152, v143
	v_rcp_f32_e32 v146, v146
	v_rcp_f32_e32 v147, v147
	v_pk_mul_f32 v[102:103], v[102:103], v[144:145]
	v_cvt_pk_f32_fp8_e32 v[144:145], v139
	v_med3_f32 v149, v149, s35, v177
	v_mul_f32_e32 v142, 0xbfb8aa3b, v142
	v_mul_f32_e32 v143, 0xbfb8aa3b, v149
	v_exp_f32_e32 v142, v142
	v_exp_f32_e32 v143, v143
	v_add_f32_e32 v149, 1.0, v152
	v_pk_add_f32 v[140:141], v[140:141], 1.0 op_sel_hi:[1,0]
	v_rcp_f32_e32 v148, v148
	v_rcp_f32_e32 v149, v149
	v_pk_mul_f32 v[140:141], v[146:147], v[140:141]
	v_cvt_pk_f32_fp8_sdwa v[138:139], v139 src0_sel:WORD_1
	v_pk_mul_f32 v[106:107], v[106:107], v[140:141]
	v_med3_f32 v141, v144, s35, v177
	v_pk_add_f32 v[142:143], v[142:143], 1.0 op_sel_hi:[1,0]
	v_mul_f32_e32 v141, 0xbfb8aa3b, v141
	v_pk_mul_f32 v[142:143], v[148:149], v[142:143]
	v_exp_f32_e32 v141, v141
	v_cvt_pk_f32_fp8_e32 v[150:151], v137
	v_cvt_pk_f32_fp8_sdwa v[136:137], v137 src0_sel:WORD_1
	v_pk_mul_f32 v[108:109], v[108:109], v[142:143]
	v_med3_f32 v143, v145, s35, v177
	v_med3_f32 v138, v138, s35, v177
	v_med3_f32 v139, v139, s35, v177
	v_mul_f32_e32 v143, 0xbfb8aa3b, v143
	v_mul_f32_e32 v138, 0xbfb8aa3b, v138
	v_mul_f32_e32 v139, 0xbfb8aa3b, v139
	v_add_f32_e32 v141, 1.0, v141
	v_exp_f32_e32 v143, v143
	v_exp_f32_e32 v138, v138
	v_exp_f32_e32 v139, v139
	v_rcp_f32_e32 v142, v141
	v_med3_f32 v140, v150, s35, v177
	v_med3_f32 v141, v151, s35, v177
	v_med3_f32 v136, v136, s35, v177
	v_med3_f32 v137, v137, s35, v177
	v_mul_f32_e32 v140, 0xbfb8aa3b, v140
	v_mul_f32_e32 v141, 0xbfb8aa3b, v141
	v_mul_f32_e32 v136, 0xbfb8aa3b, v136
	v_mul_f32_e32 v137, 0xbfb8aa3b, v137
	v_exp_f32_e32 v140, v140
	v_exp_f32_e32 v141, v141
	v_add_f32_e32 v143, 1.0, v143
	v_exp_f32_e32 v136, v136
	v_add_f32_e32 v138, 1.0, v138
	v_exp_f32_e32 v137, v137
	v_add_f32_e32 v139, 1.0, v139
	v_rcp_f32_e32 v143, v143
	v_rcp_f32_e32 v138, v138
	v_rcp_f32_e32 v139, v139
	v_pk_add_f32 v[136:137], v[136:137], 1.0 op_sel_hi:[1,0]
	v_pk_add_f32 v[140:141], v[140:141], 1.0 op_sel_hi:[1,0]
	v_pk_mul_f32 v[136:137], v[138:139], v[136:137]
	v_pk_mul_f32 v[140:141], v[142:143], v[140:141]
	v_pk_mul_f32 v[116:117], v[116:117], v[136:137]
	v_pk_mul_f32 v[114:115], v[114:115], v[140:141]
	s_nop 0
	global_load_dwordx2 v[162:163], v160, s[14:15]
	s_nop 0
	global_load_dwordx2 v[160:161], v160, s[16:17]
	v_add_u32_e32 v136, 0x1200, v134
	v_add_u32_e32 v137, 0x1400, v134
	v_add_u32_e32 v138, 0x1600, v134
	v_add_u32_e32 v139, 0x1800, v134
	v_add_u32_e32 v140, 0x1a00, v134
	v_add_u32_e32 v141, 0x1c00, v134
	v_add_u32_e32 v134, 0x1e00, v134
	global_load_dwordx2 v[178:179], v136, s[14:15]
	global_load_dwordx2 v[180:181], v136, s[16:17]
	global_load_dwordx2 v[158:159], v137, s[14:15]
	global_load_dwordx2 v[156:157], v137, s[16:17]
	global_load_dwordx2 v[154:155], v138, s[14:15]
	global_load_dwordx2 v[152:153], v138, s[16:17]
	global_load_dwordx2 v[150:151], v139, s[14:15]
	global_load_dwordx2 v[148:149], v139, s[16:17]
	global_load_dwordx2 v[146:147], v140, s[14:15]
	global_load_dwordx2 v[144:145], v140, s[16:17]
	global_load_dwordx2 v[142:143], v141, s[14:15]
	s_nop 0
	global_load_dwordx2 v[140:141], v141, s[16:17]
	s_nop 0
	global_load_dwordx2 v[138:139], v134, s[14:15]
	global_load_dwordx2 v[136:137], v134, s[16:17]
	s_waitcnt vmcnt(15)
	v_cvt_pk_f32_fp8_e32 v[182:183], v162
	s_waitcnt vmcnt(14)
	v_cvt_pk_f32_fp8_e32 v[188:189], v160
	v_cvt_pk_f32_fp8_sdwa v[184:185], v162 src0_sel:WORD_1
	v_cvt_pk_f32_fp8_sdwa v[190:191], v160 src0_sel:WORD_1
	v_med3_f32 v182, v182, s35, v177
	v_mul_f32_e32 v182, 0xbfb8aa3b, v182
	v_max_f32_e32 v134, v188, v188
	v_exp_f32_e32 v188, v182
	v_med3_f32 v134, v134, s35, v177
	v_mul_f32_e32 v134, 0xbfb8aa3b, v134
	v_med3_f32 v183, v183, s35, v177
	v_exp_f32_e32 v182, v134
	v_add_f32_e32 v134, 1.0, v188
	v_mul_f32_e32 v183, 0xbfb8aa3b, v183
	v_rcp_f32_e32 v188, v134
	v_max_f32_e32 v134, v189, v189
	v_exp_f32_e32 v189, v183
	v_med3_f32 v134, v134, s35, v177
	v_mul_f32_e32 v134, 0xbfb8aa3b, v134
	v_med3_f32 v184, v184, s35, v177
	v_exp_f32_e32 v183, v134
	v_add_f32_e32 v134, 1.0, v189
	v_mul_f32_e32 v184, 0xbfb8aa3b, v184
	v_rcp_f32_e32 v189, v134
	v_max_f32_e32 v134, v190, v190
	v_exp_f32_e32 v190, v184
	v_cvt_pk_f32_fp8_e32 v[186:187], v163
	v_med3_f32 v134, v134, s35, v177
	v_med3_f32 v185, v185, s35, v177
	v_mul_f32_e32 v134, 0xbfb8aa3b, v134
	v_mul_f32_e32 v185, 0xbfb8aa3b, v185
	v_pk_add_f32 v[182:183], v[182:183], 1.0 op_sel_hi:[1,0]
	v_exp_f32_e32 v184, v134
	v_add_f32_e32 v134, 1.0, v190
	v_max_f32_e32 v190, v191, v191
	v_exp_f32_e32 v191, v185
	v_pk_mul_f32 v[182:183], v[188:189], v[182:183]
	v_cvt_pk_f32_fp8_e32 v[192:193], v161
	v_pk_mul_f32 v[118:119], v[118:119], v[182:183]
	v_med3_f32 v182, v186, s35, v177
	v_med3_f32 v190, v190, s35, v177
	v_mul_f32_e32 v182, 0xbfb8aa3b, v182
	v_mul_f32_e32 v185, 0xbfb8aa3b, v190
	v_rcp_f32_e32 v190, v134
	v_add_f32_e32 v134, 1.0, v191
	v_exp_f32_e32 v183, v182
	v_exp_f32_e32 v185, v185
	v_rcp_f32_e32 v191, v134
	v_med3_f32 v134, v192, s35, v177
	v_mul_f32_e32 v134, 0xbfb8aa3b, v134
	v_exp_f32_e32 v182, v134
	v_add_f32_e32 v134, 1.0, v183
	v_pk_add_f32 v[184:185], v[184:185], 1.0 op_sel_hi:[1,0]
	v_med3_f32 v183, v187, s35, v177
	v_pk_mul_f32 v[184:185], v[190:191], v[184:185]
	v_mul_f32_e32 v183, 0xbfb8aa3b, v183
	v_pk_mul_f32 v[120:121], v[120:121], v[184:185]
	v_exp_f32_e32 v185, v183
	v_cvt_pk_f32_fp8_sdwa v[162:163], v163 src0_sel:WORD_1
	v_cvt_pk_f32_fp8_sdwa v[160:161], v161 src0_sel:WORD_1
	v_rcp_f32_e32 v184, v134
	v_med3_f32 v134, v193, s35, v177
	v_mul_f32_e32 v134, 0xbfb8aa3b, v134
	v_exp_f32_e32 v183, v134
	v_add_f32_e32 v134, 1.0, v185
	v_rcp_f32_e32 v185, v134
	v_max_f32_e32 v134, v160, v160
	v_med3_f32 v160, v162, s35, v177
	v_mul_f32_e32 v160, 0xbfb8aa3b, v160
	v_exp_f32_e32 v162, v160
	v_med3_f32 v134, v134, s35, v177
	v_mul_f32_e32 v134, 0xbfb8aa3b, v134
	v_exp_f32_e32 v160, v134
	v_add_f32_e32 v134, 1.0, v162
	v_med3_f32 v162, v163, s35, v177
	v_mul_f32_e32 v162, 0xbfb8aa3b, v162
	v_exp_f32_e32 v163, v162
	v_med3_f32 v161, v161, s35, v177
	v_mul_f32_e32 v161, 0xbfb8aa3b, v161
	v_exp_f32_e32 v161, v161
	v_rcp_f32_e32 v162, v134
	v_add_f32_e32 v134, 1.0, v163
	v_rcp_f32_e32 v163, v134
	v_pk_add_f32 v[160:161], v[160:161], 1.0 op_sel_hi:[1,0]
	v_pk_add_f32 v[182:183], v[182:183], 1.0 op_sel_hi:[1,0]
	s_waitcnt vmcnt(12)
	v_cvt_pk_f32_fp8_sdwa v[186:187], v180 src0_sel:WORD_1
	v_pk_mul_f32 v[160:161], v[162:163], v[160:161]
	v_pk_mul_f32 v[182:183], v[184:185], v[182:183]
	v_pk_mul_f32 v[128:129], v[128:129], v[160:161]
	v_cvt_pk_f32_fp8_e32 v[160:161], v178
	v_cvt_pk_f32_fp8_e32 v[184:185], v180
	v_cvt_pk_f32_fp8_sdwa v[162:163], v178 src0_sel:WORD_1
	v_pk_mul_f32 v[126:127], v[126:127], v[182:183]
	v_med3_f32 v160, v160, s35, v177
	v_mul_f32_e32 v160, 0xbfb8aa3b, v160
	v_max_f32_e32 v134, v184, v184
	v_exp_f32_e32 v184, v160
	v_med3_f32 v134, v134, s35, v177
	v_mul_f32_e32 v134, 0xbfb8aa3b, v134
	v_med3_f32 v161, v161, s35, v177
	v_exp_f32_e32 v160, v134
	v_add_f32_e32 v134, 1.0, v184
	v_mul_f32_e32 v161, 0xbfb8aa3b, v161
	v_rcp_f32_e32 v184, v134
	v_max_f32_e32 v134, v185, v185
	v_exp_f32_e32 v185, v161
	v_med3_f32 v134, v134, s35, v177
	v_mul_f32_e32 v134, 0xbfb8aa3b, v134
	v_med3_f32 v162, v162, s35, v177
	v_exp_f32_e32 v161, v134
	v_add_f32_e32 v134, 1.0, v185
	v_mul_f32_e32 v162, 0xbfb8aa3b, v162
	v_rcp_f32_e32 v185, v134
	v_max_f32_e32 v134, v186, v186
	v_exp_f32_e32 v186, v162
	v_cvt_pk_f32_fp8_e32 v[182:183], v179
	v_med3_f32 v134, v134, s35, v177
	v_med3_f32 v163, v163, s35, v177
	v_mul_f32_e32 v134, 0xbfb8aa3b, v134
	v_mul_f32_e32 v163, 0xbfb8aa3b, v163
	v_pk_add_f32 v[160:161], v[160:161], 1.0 op_sel_hi:[1,0]
	v_exp_f32_e32 v162, v134
	v_add_f32_e32 v134, 1.0, v186
	v_max_f32_e32 v186, v187, v187
	v_exp_f32_e32 v187, v163
	v_pk_mul_f32 v[160:161], v[184:185], v[160:161]
	v_cvt_pk_f32_fp8_e32 v[188:189], v181
	v_pk_mul_f32 v[122:123], v[122:123], v[160:161]
	v_med3_f32 v160, v182, s35, v177
	v_med3_f32 v186, v186, s35, v177
	v_mul_f32_e32 v160, 0xbfb8aa3b, v160
	v_mul_f32_e32 v163, 0xbfb8aa3b, v186
	v_rcp_f32_e32 v186, v134
	v_add_f32_e32 v134, 1.0, v187
	v_exp_f32_e32 v161, v160
	v_exp_f32_e32 v163, v163
	v_rcp_f32_e32 v187, v134
	v_med3_f32 v134, v188, s35, v177
	v_mul_f32_e32 v134, 0xbfb8aa3b, v134
	v_exp_f32_e32 v160, v134
	v_add_f32_e32 v134, 1.0, v161
	v_cvt_pk_f32_fp8_sdwa v[178:179], v179 src0_sel:WORD_1
	v_pk_add_f32 v[162:163], v[162:163], 1.0 op_sel_hi:[1,0]
	v_med3_f32 v161, v183, s35, v177
	v_pk_mul_f32 v[162:163], v[186:187], v[162:163]
	v_mul_f32_e32 v161, 0xbfb8aa3b, v161
	v_pk_mul_f32 v[124:125], v[124:125], v[162:163]
	v_exp_f32_e32 v163, v161
	v_cvt_pk_f32_fp8_sdwa v[180:181], v181 src0_sel:WORD_1
	v_rcp_f32_e32 v162, v134
	v_med3_f32 v134, v189, s35, v177
	v_mul_f32_e32 v134, 0xbfb8aa3b, v134
	v_med3_f32 v178, v178, s35, v177
	v_exp_f32_e32 v161, v134
	v_add_f32_e32 v134, 1.0, v163
	v_mul_f32_e32 v178, 0xbfb8aa3b, v178
	v_rcp_f32_e32 v163, v134
	v_max_f32_e32 v134, v180, v180
	v_exp_f32_e32 v180, v178
	v_med3_f32 v134, v134, s35, v177
	v_med3_f32 v179, v179, s35, v177
	v_mul_f32_e32 v134, 0xbfb8aa3b, v134
	v_mul_f32_e32 v179, 0xbfb8aa3b, v179
	v_exp_f32_e32 v178, v134
	v_add_f32_e32 v134, 1.0, v180
	v_max_f32_e32 v180, v181, v181
	v_exp_f32_e32 v181, v179
	v_med3_f32 v180, v180, s35, v177
	v_mul_f32_e32 v179, 0xbfb8aa3b, v180
	v_exp_f32_e32 v179, v179
	v_rcp_f32_e32 v180, v134
	v_add_f32_e32 v134, 1.0, v181
	v_pk_add_f32 v[160:161], v[160:161], 1.0 op_sel_hi:[1,0]
	v_rcp_f32_e32 v181, v134
	v_pk_mul_f32 v[160:161], v[162:163], v[160:161]
	v_pk_add_f32 v[178:179], v[178:179], 1.0 op_sel_hi:[1,0]
	v_pk_mul_f32 v[110:111], v[110:111], v[160:161]
	s_waitcnt vmcnt(11)
	v_cvt_pk_f32_fp8_e32 v[160:161], v158
	v_pk_mul_f32 v[162:163], v[180:181], v[178:179]
	s_waitcnt vmcnt(10)
	v_cvt_pk_f32_fp8_e32 v[180:181], v156
	v_pk_mul_f32 v[112:113], v[112:113], v[162:163]
	v_med3_f32 v160, v160, s35, v177
	v_mul_f32_e32 v160, 0xbfb8aa3b, v160
	v_max_f32_e32 v134, v180, v180
	v_exp_f32_e32 v180, v160
	v_med3_f32 v134, v134, s35, v177
	v_cvt_pk_f32_fp8_sdwa v[162:163], v158 src0_sel:WORD_1
	v_mul_f32_e32 v134, 0xbfb8aa3b, v134
	v_med3_f32 v161, v161, s35, v177
	v_exp_f32_e32 v160, v134
	v_add_f32_e32 v134, 1.0, v180
	v_mul_f32_e32 v161, 0xbfb8aa3b, v161
	v_rcp_f32_e32 v180, v134
	v_max_f32_e32 v134, v181, v181
	v_exp_f32_e32 v181, v161
	v_cvt_pk_f32_fp8_sdwa v[182:183], v156 src0_sel:WORD_1
	v_med3_f32 v134, v134, s35, v177
	v_mul_f32_e32 v134, 0xbfb8aa3b, v134
	v_med3_f32 v162, v162, s35, v177
	v_exp_f32_e32 v161, v134
	v_add_f32_e32 v134, 1.0, v181
	v_mul_f32_e32 v162, 0xbfb8aa3b, v162
	v_rcp_f32_e32 v181, v134
	v_max_f32_e32 v134, v182, v182
	v_exp_f32_e32 v182, v162
	v_cvt_pk_f32_fp8_e32 v[178:179], v159
	v_med3_f32 v134, v134, s35, v177
	v_med3_f32 v163, v163, s35, v177
	v_mul_f32_e32 v134, 0xbfb8aa3b, v134
	v_mul_f32_e32 v163, 0xbfb8aa3b, v163
	v_pk_add_f32 v[160:161], v[160:161], 1.0 op_sel_hi:[1,0]
	v_exp_f32_e32 v162, v134
	v_add_f32_e32 v134, 1.0, v182
	v_max_f32_e32 v182, v183, v183
	v_exp_f32_e32 v183, v163
	v_pk_mul_f32 v[160:161], v[180:181], v[160:161]
	v_cvt_pk_f32_fp8_e32 v[184:185], v157
	v_pk_mul_f32 v[98:99], v[98:99], v[160:161]
	v_med3_f32 v160, v178, s35, v177
	v_med3_f32 v182, v182, s35, v177
	v_mul_f32_e32 v160, 0xbfb8aa3b, v160
	v_mul_f32_e32 v163, 0xbfb8aa3b, v182
	v_rcp_f32_e32 v182, v134
	v_add_f32_e32 v134, 1.0, v183
	v_exp_f32_e32 v161, v160
	v_exp_f32_e32 v163, v163
	v_rcp_f32_e32 v183, v134
	v_med3_f32 v134, v184, s35, v177
	v_mul_f32_e32 v134, 0xbfb8aa3b, v134
	v_exp_f32_e32 v160, v134
	v_add_f32_e32 v134, 1.0, v161
	v_pk_add_f32 v[162:163], v[162:163], 1.0 op_sel_hi:[1,0]
	v_med3_f32 v161, v179, s35, v177
	v_pk_mul_f32 v[162:163], v[182:183], v[162:163]
	v_mul_f32_e32 v161, 0xbfb8aa3b, v161
	v_pk_mul_f32 v[100:101], v[100:101], v[162:163]
	v_exp_f32_e32 v163, v161
	v_cvt_pk_f32_fp8_sdwa v[158:159], v159 src0_sel:WORD_1
	v_cvt_pk_f32_fp8_sdwa v[156:157], v157 src0_sel:WORD_1
	v_rcp_f32_e32 v162, v134
	v_med3_f32 v134, v185, s35, v177
	v_mul_f32_e32 v134, 0xbfb8aa3b, v134
	v_exp_f32_e32 v161, v134
	v_add_f32_e32 v134, 1.0, v163
	v_rcp_f32_e32 v163, v134
	v_max_f32_e32 v134, v156, v156
	v_med3_f32 v156, v158, s35, v177
	v_mul_f32_e32 v156, 0xbfb8aa3b, v156
	v_exp_f32_e32 v158, v156
	v_med3_f32 v134, v134, s35, v177
	v_mul_f32_e32 v134, 0xbfb8aa3b, v134
	v_exp_f32_e32 v156, v134
	v_add_f32_e32 v134, 1.0, v158
	v_med3_f32 v158, v159, s35, v177
	v_mul_f32_e32 v158, 0xbfb8aa3b, v158
	v_exp_f32_e32 v159, v158
	v_med3_f32 v157, v157, s35, v177
	v_mul_f32_e32 v157, 0xbfb8aa3b, v157
	v_exp_f32_e32 v157, v157
	v_rcp_f32_e32 v158, v134
	v_add_f32_e32 v134, 1.0, v159
	v_rcp_f32_e32 v159, v134
	v_pk_add_f32 v[156:157], v[156:157], 1.0 op_sel_hi:[1,0]
	v_pk_add_f32 v[160:161], v[160:161], 1.0 op_sel_hi:[1,0]
	s_waitcnt vmcnt(8)
	v_cvt_pk_f32_fp8_sdwa v[178:179], v152 src0_sel:WORD_1
	v_pk_mul_f32 v[156:157], v[158:159], v[156:157]
	v_pk_mul_f32 v[160:161], v[162:163], v[160:161]
	v_pk_mul_f32 v[88:89], v[88:89], v[156:157]
	v_cvt_pk_f32_fp8_e32 v[156:157], v154
	v_cvt_pk_f32_fp8_e32 v[162:163], v152
	v_cvt_pk_f32_fp8_sdwa v[158:159], v154 src0_sel:WORD_1
	v_pk_mul_f32 v[86:87], v[86:87], v[160:161]
	v_med3_f32 v156, v156, s35, v177
	v_mul_f32_e32 v156, 0xbfb8aa3b, v156
	v_max_f32_e32 v134, v162, v162
	v_exp_f32_e32 v162, v156
	v_med3_f32 v134, v134, s35, v177
	v_mul_f32_e32 v134, 0xbfb8aa3b, v134
	v_med3_f32 v157, v157, s35, v177
	v_exp_f32_e32 v156, v134
	v_add_f32_e32 v134, 1.0, v162
	v_mul_f32_e32 v157, 0xbfb8aa3b, v157
	v_rcp_f32_e32 v162, v134
	v_max_f32_e32 v134, v163, v163
	v_exp_f32_e32 v163, v157
	v_med3_f32 v134, v134, s35, v177
	v_mul_f32_e32 v134, 0xbfb8aa3b, v134
	v_med3_f32 v158, v158, s35, v177
	v_exp_f32_e32 v157, v134
	v_add_f32_e32 v134, 1.0, v163
	v_mul_f32_e32 v158, 0xbfb8aa3b, v158
	v_rcp_f32_e32 v163, v134
	v_max_f32_e32 v134, v178, v178
	v_exp_f32_e32 v178, v158
	v_cvt_pk_f32_fp8_e32 v[160:161], v155
	v_med3_f32 v134, v134, s35, v177
	v_med3_f32 v159, v159, s35, v177
	v_mul_f32_e32 v134, 0xbfb8aa3b, v134
	v_mul_f32_e32 v159, 0xbfb8aa3b, v159
	v_pk_add_f32 v[156:157], v[156:157], 1.0 op_sel_hi:[1,0]
	v_exp_f32_e32 v158, v134
	v_add_f32_e32 v134, 1.0, v178
	v_max_f32_e32 v178, v179, v179
	v_exp_f32_e32 v179, v159
	v_pk_mul_f32 v[156:157], v[162:163], v[156:157]
	v_cvt_pk_f32_fp8_e32 v[180:181], v153
	v_pk_mul_f32 v[70:71], v[70:71], v[156:157]
	v_med3_f32 v156, v160, s35, v177
	v_med3_f32 v178, v178, s35, v177
	v_mul_f32_e32 v156, 0xbfb8aa3b, v156
	v_mul_f32_e32 v159, 0xbfb8aa3b, v178
	v_rcp_f32_e32 v178, v134
	v_add_f32_e32 v134, 1.0, v179
	v_exp_f32_e32 v157, v156
	v_exp_f32_e32 v159, v159
	v_rcp_f32_e32 v179, v134
	v_med3_f32 v134, v180, s35, v177
	v_mul_f32_e32 v134, 0xbfb8aa3b, v134
	v_exp_f32_e32 v156, v134
	v_add_f32_e32 v134, 1.0, v157
	v_pk_add_f32 v[158:159], v[158:159], 1.0 op_sel_hi:[1,0]
	v_med3_f32 v157, v161, s35, v177
	v_pk_mul_f32 v[158:159], v[178:179], v[158:159]
	v_mul_f32_e32 v157, 0xbfb8aa3b, v157
	v_pk_mul_f32 v[72:73], v[72:73], v[158:159]
	v_exp_f32_e32 v159, v157
	v_cvt_pk_f32_fp8_sdwa v[154:155], v155 src0_sel:WORD_1
	v_cvt_pk_f32_fp8_sdwa v[152:153], v153 src0_sel:WORD_1
	v_rcp_f32_e32 v158, v134
	v_med3_f32 v134, v181, s35, v177
	v_mul_f32_e32 v134, 0xbfb8aa3b, v134
	v_exp_f32_e32 v157, v134
	v_add_f32_e32 v134, 1.0, v159
	v_rcp_f32_e32 v159, v134
	v_max_f32_e32 v134, v152, v152
	v_med3_f32 v152, v154, s35, v177
	v_mul_f32_e32 v152, 0xbfb8aa3b, v152
	v_exp_f32_e32 v154, v152
	v_med3_f32 v134, v134, s35, v177
	v_mul_f32_e32 v134, 0xbfb8aa3b, v134
	v_exp_f32_e32 v152, v134
	v_add_f32_e32 v134, 1.0, v154
	v_med3_f32 v154, v155, s35, v177
	v_mul_f32_e32 v154, 0xbfb8aa3b, v154
	v_exp_f32_e32 v155, v154
	v_med3_f32 v153, v153, s35, v177
	v_mul_f32_e32 v153, 0xbfb8aa3b, v153
	v_exp_f32_e32 v153, v153
	v_rcp_f32_e32 v154, v134
	v_add_f32_e32 v134, 1.0, v155
	v_rcp_f32_e32 v155, v134
	v_pk_add_f32 v[152:153], v[152:153], 1.0 op_sel_hi:[1,0]
	v_pk_add_f32 v[156:157], v[156:157], 1.0 op_sel_hi:[1,0]
	s_waitcnt vmcnt(6)
	v_cvt_pk_f32_fp8_sdwa v[160:161], v148 src0_sel:WORD_1
	v_pk_mul_f32 v[152:153], v[154:155], v[152:153]
	v_pk_mul_f32 v[156:157], v[158:159], v[156:157]
	v_pk_mul_f32 v[60:61], v[60:61], v[152:153]
	v_cvt_pk_f32_fp8_e32 v[152:153], v150
	v_cvt_pk_f32_fp8_e32 v[158:159], v148
	v_cvt_pk_f32_fp8_sdwa v[154:155], v150 src0_sel:WORD_1
	v_pk_mul_f32 v[58:59], v[58:59], v[156:157]
	v_med3_f32 v152, v152, s35, v177
	v_mul_f32_e32 v152, 0xbfb8aa3b, v152
	v_max_f32_e32 v134, v158, v158
	v_exp_f32_e32 v158, v152
	v_med3_f32 v134, v134, s35, v177
	v_mul_f32_e32 v134, 0xbfb8aa3b, v134
	v_med3_f32 v153, v153, s35, v177
	v_exp_f32_e32 v152, v134
	v_add_f32_e32 v134, 1.0, v158
	v_mul_f32_e32 v153, 0xbfb8aa3b, v153
	v_rcp_f32_e32 v158, v134
	v_max_f32_e32 v134, v159, v159
	v_exp_f32_e32 v159, v153
	v_med3_f32 v134, v134, s35, v177
	v_mul_f32_e32 v134, 0xbfb8aa3b, v134
	v_med3_f32 v154, v154, s35, v177
	v_exp_f32_e32 v153, v134
	v_add_f32_e32 v134, 1.0, v159
	v_mul_f32_e32 v154, 0xbfb8aa3b, v154
	v_rcp_f32_e32 v159, v134
	v_max_f32_e32 v134, v160, v160
	v_exp_f32_e32 v160, v154
	v_cvt_pk_f32_fp8_e32 v[156:157], v151
	v_med3_f32 v134, v134, s35, v177
	v_med3_f32 v155, v155, s35, v177
	v_mul_f32_e32 v134, 0xbfb8aa3b, v134
	v_mul_f32_e32 v155, 0xbfb8aa3b, v155
	v_pk_add_f32 v[152:153], v[152:153], 1.0 op_sel_hi:[1,0]
	v_exp_f32_e32 v154, v134
	v_add_f32_e32 v134, 1.0, v160
	v_max_f32_e32 v160, v161, v161
	v_exp_f32_e32 v161, v155
	v_pk_mul_f32 v[152:153], v[158:159], v[152:153]
	v_cvt_pk_f32_fp8_e32 v[162:163], v149
	v_pk_mul_f32 v[46:47], v[46:47], v[152:153]
	v_med3_f32 v152, v156, s35, v177
	v_med3_f32 v160, v160, s35, v177
	v_mul_f32_e32 v152, 0xbfb8aa3b, v152
	v_mul_f32_e32 v155, 0xbfb8aa3b, v160
	v_rcp_f32_e32 v160, v134
	v_add_f32_e32 v134, 1.0, v161
	v_exp_f32_e32 v153, v152
	v_exp_f32_e32 v155, v155
	v_rcp_f32_e32 v161, v134
	v_med3_f32 v134, v162, s35, v177
	v_mul_f32_e32 v134, 0xbfb8aa3b, v134
	v_exp_f32_e32 v152, v134
	v_add_f32_e32 v134, 1.0, v153
	v_pk_add_f32 v[154:155], v[154:155], 1.0 op_sel_hi:[1,0]
	v_med3_f32 v153, v157, s35, v177
	v_pk_mul_f32 v[154:155], v[160:161], v[154:155]
	v_mul_f32_e32 v153, 0xbfb8aa3b, v153
	v_pk_mul_f32 v[48:49], v[48:49], v[154:155]
	v_exp_f32_e32 v155, v153
	v_cvt_pk_f32_fp8_sdwa v[150:151], v151 src0_sel:WORD_1
	v_cvt_pk_f32_fp8_sdwa v[148:149], v149 src0_sel:WORD_1
	v_rcp_f32_e32 v154, v134
	v_med3_f32 v134, v163, s35, v177
	v_mul_f32_e32 v134, 0xbfb8aa3b, v134
	v_exp_f32_e32 v153, v134
	v_add_f32_e32 v134, 1.0, v155
	v_rcp_f32_e32 v155, v134
	v_max_f32_e32 v134, v148, v148
	v_med3_f32 v148, v150, s35, v177
	v_mul_f32_e32 v148, 0xbfb8aa3b, v148
	v_exp_f32_e32 v150, v148
	v_med3_f32 v134, v134, s35, v177
	v_mul_f32_e32 v134, 0xbfb8aa3b, v134
	v_exp_f32_e32 v148, v134
	v_add_f32_e32 v134, 1.0, v150
	v_med3_f32 v150, v151, s35, v177
	v_mul_f32_e32 v150, 0xbfb8aa3b, v150
	v_exp_f32_e32 v151, v150
	v_med3_f32 v149, v149, s35, v177
	v_mul_f32_e32 v149, 0xbfb8aa3b, v149
	v_exp_f32_e32 v149, v149
	v_rcp_f32_e32 v150, v134
	v_add_f32_e32 v134, 1.0, v151
	v_rcp_f32_e32 v151, v134
	v_pk_add_f32 v[148:149], v[148:149], 1.0 op_sel_hi:[1,0]
	v_pk_add_f32 v[152:153], v[152:153], 1.0 op_sel_hi:[1,0]
	s_waitcnt vmcnt(4)
	v_cvt_pk_f32_fp8_sdwa v[156:157], v144 src0_sel:WORD_1
	v_pk_mul_f32 v[148:149], v[150:151], v[148:149]
	v_pk_mul_f32 v[152:153], v[154:155], v[152:153]
	v_pk_mul_f32 v[36:37], v[36:37], v[148:149]
	v_cvt_pk_f32_fp8_e32 v[148:149], v146
	v_cvt_pk_f32_fp8_e32 v[154:155], v144
	v_cvt_pk_f32_fp8_sdwa v[150:151], v146 src0_sel:WORD_1
	v_pk_mul_f32 v[34:35], v[34:35], v[152:153]
	v_med3_f32 v148, v148, s35, v177
	v_mul_f32_e32 v148, 0xbfb8aa3b, v148
	v_max_f32_e32 v134, v154, v154
	v_exp_f32_e32 v154, v148
	v_med3_f32 v134, v134, s35, v177
	v_mul_f32_e32 v134, 0xbfb8aa3b, v134
	v_med3_f32 v149, v149, s35, v177
	v_exp_f32_e32 v148, v134
	v_add_f32_e32 v134, 1.0, v154
	v_mul_f32_e32 v149, 0xbfb8aa3b, v149
	v_rcp_f32_e32 v154, v134
	v_max_f32_e32 v134, v155, v155
	v_exp_f32_e32 v155, v149
	v_med3_f32 v134, v134, s35, v177
	v_mul_f32_e32 v134, 0xbfb8aa3b, v134
	v_med3_f32 v150, v150, s35, v177
	v_exp_f32_e32 v149, v134
	v_add_f32_e32 v134, 1.0, v155
	v_mul_f32_e32 v150, 0xbfb8aa3b, v150
	v_rcp_f32_e32 v155, v134
	v_max_f32_e32 v134, v156, v156
	v_exp_f32_e32 v156, v150
	v_cvt_pk_f32_fp8_e32 v[152:153], v147
	v_med3_f32 v134, v134, s35, v177
	v_med3_f32 v151, v151, s35, v177
	v_mul_f32_e32 v134, 0xbfb8aa3b, v134
	v_mul_f32_e32 v151, 0xbfb8aa3b, v151
	v_pk_add_f32 v[148:149], v[148:149], 1.0 op_sel_hi:[1,0]
	v_exp_f32_e32 v150, v134
	v_add_f32_e32 v134, 1.0, v156
	v_max_f32_e32 v156, v157, v157
	v_exp_f32_e32 v157, v151
	v_pk_mul_f32 v[148:149], v[154:155], v[148:149]
	v_cvt_pk_f32_fp8_e32 v[158:159], v145
	v_pk_mul_f32 v[22:23], v[22:23], v[148:149]
	v_med3_f32 v148, v152, s35, v177
	v_med3_f32 v156, v156, s35, v177
	v_mul_f32_e32 v148, 0xbfb8aa3b, v148
	v_mul_f32_e32 v151, 0xbfb8aa3b, v156
	v_rcp_f32_e32 v156, v134
	v_add_f32_e32 v134, 1.0, v157
	v_exp_f32_e32 v149, v148
	v_exp_f32_e32 v151, v151
	v_rcp_f32_e32 v157, v134
	v_med3_f32 v134, v158, s35, v177
	v_mul_f32_e32 v134, 0xbfb8aa3b, v134
	v_exp_f32_e32 v148, v134
	v_add_f32_e32 v134, 1.0, v149
	v_pk_add_f32 v[150:151], v[150:151], 1.0 op_sel_hi:[1,0]
	v_med3_f32 v149, v153, s35, v177
	v_pk_mul_f32 v[150:151], v[156:157], v[150:151]
	v_mul_f32_e32 v149, 0xbfb8aa3b, v149
	v_pk_mul_f32 v[24:25], v[24:25], v[150:151]
	v_exp_f32_e32 v151, v149
	v_cvt_pk_f32_fp8_sdwa v[146:147], v147 src0_sel:WORD_1
	v_cvt_pk_f32_fp8_sdwa v[144:145], v145 src0_sel:WORD_1
	v_rcp_f32_e32 v150, v134
	v_med3_f32 v134, v159, s35, v177
	v_mul_f32_e32 v134, 0xbfb8aa3b, v134
	v_exp_f32_e32 v149, v134
	v_add_f32_e32 v134, 1.0, v151
	v_rcp_f32_e32 v151, v134
	v_max_f32_e32 v134, v144, v144
	v_med3_f32 v144, v146, s35, v177
	v_mul_f32_e32 v144, 0xbfb8aa3b, v144
	v_exp_f32_e32 v146, v144
	v_med3_f32 v134, v134, s35, v177
	v_mul_f32_e32 v134, 0xbfb8aa3b, v134
	v_exp_f32_e32 v144, v134
	v_add_f32_e32 v134, 1.0, v146
	v_med3_f32 v146, v147, s35, v177
	v_mul_f32_e32 v146, 0xbfb8aa3b, v146
	v_exp_f32_e32 v147, v146
	v_med3_f32 v145, v145, s35, v177
	v_mul_f32_e32 v145, 0xbfb8aa3b, v145
	v_exp_f32_e32 v145, v145
	v_rcp_f32_e32 v146, v134
	v_add_f32_e32 v134, 1.0, v147
	v_rcp_f32_e32 v147, v134
	v_pk_add_f32 v[144:145], v[144:145], 1.0 op_sel_hi:[1,0]
	v_pk_add_f32 v[148:149], v[148:149], 1.0 op_sel_hi:[1,0]
	s_waitcnt vmcnt(2)
	v_cvt_pk_f32_fp8_sdwa v[152:153], v140 src0_sel:WORD_1
	v_pk_mul_f32 v[144:145], v[146:147], v[144:145]
	v_pk_mul_f32 v[148:149], v[150:151], v[148:149]
	v_pk_mul_f32 v[20:21], v[20:21], v[144:145]
	v_cvt_pk_f32_fp8_e32 v[144:145], v142
	v_cvt_pk_f32_fp8_e32 v[150:151], v140
	v_cvt_pk_f32_fp8_sdwa v[146:147], v142 src0_sel:WORD_1
	v_pk_mul_f32 v[18:19], v[18:19], v[148:149]
	v_med3_f32 v144, v144, s35, v177
	v_mul_f32_e32 v144, 0xbfb8aa3b, v144
	v_max_f32_e32 v134, v150, v150
	v_exp_f32_e32 v150, v144
	v_med3_f32 v134, v134, s35, v177
	v_mul_f32_e32 v134, 0xbfb8aa3b, v134
	v_med3_f32 v145, v145, s35, v177
	v_exp_f32_e32 v144, v134
	v_add_f32_e32 v134, 1.0, v150
	v_mul_f32_e32 v145, 0xbfb8aa3b, v145
	v_rcp_f32_e32 v150, v134
	v_max_f32_e32 v134, v151, v151
	v_exp_f32_e32 v151, v145
	v_med3_f32 v134, v134, s35, v177
	v_mul_f32_e32 v134, 0xbfb8aa3b, v134
	v_med3_f32 v146, v146, s35, v177
	v_exp_f32_e32 v145, v134
	v_add_f32_e32 v134, 1.0, v151
	v_mul_f32_e32 v146, 0xbfb8aa3b, v146
	v_rcp_f32_e32 v151, v134
	v_max_f32_e32 v134, v152, v152
	v_exp_f32_e32 v152, v146
	v_cvt_pk_f32_fp8_e32 v[148:149], v143
	v_med3_f32 v134, v134, s35, v177
	v_med3_f32 v147, v147, s35, v177
	v_mul_f32_e32 v134, 0xbfb8aa3b, v134
	v_mul_f32_e32 v147, 0xbfb8aa3b, v147
	v_pk_add_f32 v[144:145], v[144:145], 1.0 op_sel_hi:[1,0]
	v_exp_f32_e32 v146, v134
	v_add_f32_e32 v134, 1.0, v152
	v_max_f32_e32 v152, v153, v153
	v_exp_f32_e32 v153, v147
	v_pk_mul_f32 v[144:145], v[150:151], v[144:145]
	v_cvt_pk_f32_fp8_e32 v[154:155], v141
	v_pk_mul_f32 v[14:15], v[14:15], v[144:145]
	v_med3_f32 v144, v148, s35, v177
	v_med3_f32 v152, v152, s35, v177
	v_mul_f32_e32 v144, 0xbfb8aa3b, v144
	v_mul_f32_e32 v147, 0xbfb8aa3b, v152
	v_rcp_f32_e32 v152, v134
	v_add_f32_e32 v134, 1.0, v153
	v_exp_f32_e32 v145, v144
	v_exp_f32_e32 v147, v147
	v_rcp_f32_e32 v153, v134
	v_med3_f32 v134, v154, s35, v177
	v_mul_f32_e32 v134, 0xbfb8aa3b, v134
	v_exp_f32_e32 v144, v134
	v_add_f32_e32 v134, 1.0, v145
	v_pk_add_f32 v[146:147], v[146:147], 1.0 op_sel_hi:[1,0]
	v_med3_f32 v145, v149, s35, v177
	v_pk_mul_f32 v[146:147], v[152:153], v[146:147]
	v_mul_f32_e32 v145, 0xbfb8aa3b, v145
	v_pk_mul_f32 v[16:17], v[16:17], v[146:147]
	v_exp_f32_e32 v147, v145
	v_cvt_pk_f32_fp8_sdwa v[142:143], v143 src0_sel:WORD_1
	v_cvt_pk_f32_fp8_sdwa v[140:141], v141 src0_sel:WORD_1
	v_rcp_f32_e32 v146, v134
	v_med3_f32 v134, v155, s35, v177
	v_mul_f32_e32 v134, 0xbfb8aa3b, v134
	v_exp_f32_e32 v145, v134
	v_add_f32_e32 v134, 1.0, v147
	v_rcp_f32_e32 v147, v134
	v_max_f32_e32 v134, v140, v140
	v_med3_f32 v140, v142, s35, v177
	v_mul_f32_e32 v140, 0xbfb8aa3b, v140
	v_exp_f32_e32 v142, v140
	v_med3_f32 v134, v134, s35, v177
	v_mul_f32_e32 v134, 0xbfb8aa3b, v134
	v_exp_f32_e32 v140, v134
	v_add_f32_e32 v134, 1.0, v142
	v_med3_f32 v142, v143, s35, v177
	v_mul_f32_e32 v142, 0xbfb8aa3b, v142
	v_exp_f32_e32 v143, v142
	v_med3_f32 v141, v141, s35, v177
	v_mul_f32_e32 v141, 0xbfb8aa3b, v141
	v_exp_f32_e32 v141, v141
	v_rcp_f32_e32 v142, v134
	v_add_f32_e32 v134, 1.0, v143
	v_rcp_f32_e32 v143, v134
	v_pk_add_f32 v[140:141], v[140:141], 1.0 op_sel_hi:[1,0]
	v_pk_add_f32 v[144:145], v[144:145], 1.0 op_sel_hi:[1,0]
	s_waitcnt vmcnt(0)
	v_cvt_pk_f32_fp8_sdwa v[148:149], v136 src0_sel:WORD_1
	v_pk_mul_f32 v[140:141], v[142:143], v[140:141]
	v_pk_mul_f32 v[144:145], v[146:147], v[144:145]
	v_pk_mul_f32 v[12:13], v[12:13], v[140:141]
	v_cvt_pk_f32_fp8_e32 v[140:141], v138
	v_cvt_pk_f32_fp8_e32 v[146:147], v136
	v_cvt_pk_f32_fp8_sdwa v[142:143], v138 src0_sel:WORD_1
	v_pk_mul_f32 v[10:11], v[10:11], v[144:145]
	v_med3_f32 v140, v140, s35, v177
	v_mul_f32_e32 v140, 0xbfb8aa3b, v140
	v_max_f32_e32 v134, v146, v146
	v_exp_f32_e32 v146, v140
	v_med3_f32 v134, v134, s35, v177
	v_mul_f32_e32 v134, 0xbfb8aa3b, v134
	v_med3_f32 v141, v141, s35, v177
	v_exp_f32_e32 v140, v134
	v_add_f32_e32 v134, 1.0, v146
	v_mul_f32_e32 v141, 0xbfb8aa3b, v141
	v_rcp_f32_e32 v146, v134
	v_max_f32_e32 v134, v147, v147
	v_exp_f32_e32 v147, v141
	v_med3_f32 v134, v134, s35, v177
	v_mul_f32_e32 v134, 0xbfb8aa3b, v134
	v_med3_f32 v142, v142, s35, v177
	v_exp_f32_e32 v141, v134
	v_add_f32_e32 v134, 1.0, v147
	v_mul_f32_e32 v142, 0xbfb8aa3b, v142
	v_rcp_f32_e32 v147, v134
	v_max_f32_e32 v134, v148, v148
	v_exp_f32_e32 v148, v142
	v_cvt_pk_f32_fp8_e32 v[144:145], v139
	v_med3_f32 v134, v134, s35, v177
	v_med3_f32 v143, v143, s35, v177
	v_mul_f32_e32 v134, 0xbfb8aa3b, v134
	v_mul_f32_e32 v143, 0xbfb8aa3b, v143
	v_pk_add_f32 v[140:141], v[140:141], 1.0 op_sel_hi:[1,0]
	v_exp_f32_e32 v142, v134
	v_add_f32_e32 v134, 1.0, v148
	v_max_f32_e32 v148, v149, v149
	v_exp_f32_e32 v149, v143
	v_pk_mul_f32 v[140:141], v[146:147], v[140:141]
	v_cvt_pk_f32_fp8_e32 v[150:151], v137
	v_pk_mul_f32 v[6:7], v[6:7], v[140:141]
	v_med3_f32 v140, v144, s35, v177
	v_med3_f32 v148, v148, s35, v177
	v_mul_f32_e32 v140, 0xbfb8aa3b, v140
	v_mul_f32_e32 v143, 0xbfb8aa3b, v148
	v_rcp_f32_e32 v148, v134
	v_add_f32_e32 v134, 1.0, v149
	v_exp_f32_e32 v141, v140
	v_exp_f32_e32 v143, v143
	v_rcp_f32_e32 v149, v134
	v_med3_f32 v134, v150, s35, v177
	v_mul_f32_e32 v134, 0xbfb8aa3b, v134
	v_exp_f32_e32 v140, v134
	v_add_f32_e32 v134, 1.0, v141
	v_pk_add_f32 v[142:143], v[142:143], 1.0 op_sel_hi:[1,0]
	v_med3_f32 v141, v145, s35, v177
	v_pk_mul_f32 v[142:143], v[148:149], v[142:143]
	v_mul_f32_e32 v141, 0xbfb8aa3b, v141
	v_pk_mul_f32 v[8:9], v[8:9], v[142:143]
	v_exp_f32_e32 v143, v141
	v_cvt_pk_f32_fp8_sdwa v[138:139], v139 src0_sel:WORD_1
	v_cvt_pk_f32_fp8_sdwa v[136:137], v137 src0_sel:WORD_1
	v_rcp_f32_e32 v142, v134
	v_med3_f32 v134, v151, s35, v177
	v_mul_f32_e32 v134, 0xbfb8aa3b, v134
	v_exp_f32_e32 v141, v134
	v_add_f32_e32 v134, 1.0, v143
	v_rcp_f32_e32 v143, v134
	v_max_f32_e32 v134, v136, v136
	v_med3_f32 v136, v138, s35, v177
	v_mul_f32_e32 v136, 0xbfb8aa3b, v136
	v_exp_f32_e32 v138, v136
	v_med3_f32 v134, v134, s35, v177
	v_mul_f32_e32 v134, 0xbfb8aa3b, v134
	v_exp_f32_e32 v136, v134
	v_add_f32_e32 v134, 1.0, v138
	v_med3_f32 v138, v139, s35, v177
	v_mul_f32_e32 v138, 0xbfb8aa3b, v138
	v_exp_f32_e32 v139, v138
	v_med3_f32 v137, v137, s35, v177
	v_mul_f32_e32 v137, 0xbfb8aa3b, v137
	v_exp_f32_e32 v137, v137
	v_rcp_f32_e32 v138, v134
	v_add_f32_e32 v134, 1.0, v139
	v_rcp_f32_e32 v139, v134
	v_pk_add_f32 v[136:137], v[136:137], 1.0 op_sel_hi:[1,0]
	v_pk_add_f32 v[140:141], v[140:141], 1.0 op_sel_hi:[1,0]
	v_pk_mul_f32 v[136:137], v[138:139], v[136:137]
	v_pk_mul_f32 v[140:141], v[142:143], v[140:141]
	v_pk_mul_f32 v[4:5], v[4:5], v[136:137]
	v_pk_mul_f32 v[2:3], v[2:3], v[140:141]
	s_nop 0

.LBB0_1051:
	v_mov_b32_e32 v134, v170
	v_mov_b32_e32 v136, v169
	s_lshl_b32 s2, s60, 8
	s_add_i32 s2, s2, s87
	v_add_lshl_u32 v136, s2, v136, 10
	s_or_b32 s2, s23, s91
	v_lshlrev_b32_e32 v134, 3, v134
	v_add3_u32 v134, s2, v134, v136
	s_lshl_b32 s32, s23, 8
	v_add_u32_e32 v216, s32, v214
	s_lshl_b32 s32, s60, 18
	v_add_u32_e32 v216, s32, v216
	v_add_u32_e32 v217, 0x1000, v216
	global_load_dwordx2 v[178:179], v216, s[16:17]
	global_load_dwordx2 v[182:183], v216, s[16:17] offset:512
	v_lshl_add_u64 v[136:137], s[16:17], 0, v[134:135]
	v_add_co_u32_e32 v138, vcc, 0x4000, v136
	s_mov_b32 s2, 0x8000
	s_nop 0
	v_addc_co_u32_e32 v139, vcc, 0, v137, vcc
	v_add_co_u32_e32 v140, vcc, 0x8000, v136
	s_waitcnt vmcnt(1)
	v_cvt_pk_f32_fp8_e32 v[180:181], v178
	v_addc_co_u32_e32 v141, vcc, 0, v137, vcc
	global_load_dwordx2 v[162:163], v216, s[16:17] offset:1024
	global_load_dwordx2 v[160:161], v216, s[16:17] offset:1536
	global_load_dwordx2 v[158:159], v216, s[16:17] offset:2048
	global_load_dwordx2 v[156:157], v216, s[16:17] offset:2560
	v_cvt_pk_f32_fp8_sdwa v[184:185], v178 src0_sel:WORD_1
	v_cvt_pk_f32_fp8_e32 v[186:187], v179
	v_cvt_pk_f32_fp8_sdwa v[178:179], v179 src0_sel:WORD_1
	v_med3_f32 v180, v180, s35, v177
	v_med3_f32 v181, v181, s35, v177
	v_med3_f32 v184, v184, s35, v177
	v_med3_f32 v185, v185, s35, v177
	v_mul_f32_e32 v180, 0xbfb8aa3b, v180
	v_mul_f32_e32 v181, 0xbfb8aa3b, v181
	v_mul_f32_e32 v184, 0xbfb8aa3b, v184
	v_mul_f32_e32 v185, 0xbfb8aa3b, v185
	v_exp_f32_e32 v180, v180
	v_exp_f32_e32 v181, v181
	v_exp_f32_e32 v184, v184
	v_exp_f32_e32 v185, v185
	v_med3_f32 v178, v178, s35, v177
	v_mul_f32_e32 v178, 0xbfb8aa3b, v178
	v_med3_f32 v179, v179, s35, v177
	v_med3_f32 v186, v186, s35, v177
	v_med3_f32 v187, v187, s35, v177
	v_add_f32_e32 v180, 1.0, v180
	v_add_f32_e32 v181, 1.0, v181
	v_exp_f32_e32 v178, v178
	v_mul_f32_e32 v179, 0xbfb8aa3b, v179
	v_mul_f32_e32 v186, 0xbfb8aa3b, v186
	v_mul_f32_e32 v187, 0xbfb8aa3b, v187
	v_add_f32_e32 v184, 1.0, v184
	v_add_f32_e32 v185, 1.0, v185
	v_rcp_f32_e32 v180, v180
	v_rcp_f32_e32 v181, v181
	v_exp_f32_e32 v179, v179
	v_exp_f32_e32 v186, v186
	v_exp_f32_e32 v187, v187
	v_rcp_f32_e32 v184, v184
	v_rcp_f32_e32 v185, v185
	v_add_f32_e32 v178, 1.0, v178
	v_rcp_f32_e32 v188, v178
	v_add_f32_e32 v178, 1.0, v179
	v_pk_mul_f32 v[26:27], v[26:27], v[180:181]
	v_add_co_u32_e32 v142, vcc, 0xc000, v136
	v_add_f32_e32 v186, 1.0, v186
	v_add_f32_e32 v187, 1.0, v187
	v_rcp_f32_e32 v189, v178
	v_cvt_pk_bf16_f32 v178, v26, v27
	v_pk_mul_f32 v[26:27], v[28:29], v[184:185]
	s_waitcnt vmcnt(4)
	v_cvt_pk_f32_fp8_e32 v[28:29], v182
	v_addc_co_u32_e32 v143, vcc, 0, v137, vcc
	v_rcp_f32_e32 v186, v186
	v_rcp_f32_e32 v187, v187
	v_add_co_u32_e32 v138, vcc, 0x20000, v136
	s_nop 0
	v_addc_co_u32_e32 v139, vcc, 0, v137, vcc
	v_add_co_u32_e32 v140, vcc, 0x24000, v136
	v_cvt_pk_bf16_f32 v179, v26, v27
	s_nop 0
	v_addc_co_u32_e32 v141, vcc, 0, v137, vcc
	v_pk_mul_f32 v[26:27], v[30:31], v[186:187]
	v_med3_f32 v28, v28, s35, v177
	global_load_dwordx2 v[154:155], v216, s[16:17] offset:3072
	global_load_dwordx2 v[152:153], v216, s[16:17] offset:3584
	global_load_dwordx2 v[150:151], v217, s[16:17]
	global_load_dwordx2 v[148:149], v217, s[16:17] offset:512
	v_add_co_u32_e32 v138, vcc, 0x28000, v136
	v_cvt_pk_bf16_f32 v180, v26, v27
	v_pk_mul_f32 v[26:27], v[32:33], v[188:189]
	v_mul_f32_e32 v28, 0xbfb8aa3b, v28
	v_addc_co_u32_e32 v139, vcc, 0, v137, vcc
	v_cvt_pk_bf16_f32 v181, v26, v27
	v_lshl_add_u64 v[26:27], v[134:135], 1, s[18:19]
	v_exp_f32_e32 v134, v28
	v_add_co_u32_e32 v136, vcc, 0x2c000, v136
	v_med3_f32 v28, v29, s35, v177
	s_nop 0
	v_addc_co_u32_e32 v137, vcc, 0, v137, vcc
	v_mul_f32_e32 v28, 0xbfb8aa3b, v28
	global_load_dwordx2 v[146:147], v217, s[16:17] offset:1024
	global_load_dwordx2 v[144:145], v217, s[16:17] offset:1536
	global_load_dwordx2 v[142:143], v217, s[16:17] offset:2048
	s_nop 0
	global_load_dwordx2 v[140:141], v217, s[16:17] offset:2560
	s_nop 0
	global_load_dwordx2 v[138:139], v217, s[16:17] offset:3072
	s_nop 0
	global_load_dwordx2 v[136:137], v217, s[16:17] offset:3584
	v_cvt_pk_f32_fp8_sdwa v[30:31], v182 src0_sel:WORD_1
	global_store_dwordx4 v[26:27], v[178:181], off
	v_cvt_pk_f32_fp8_e32 v[32:33], v183
	v_add_f32_e32 v134, 1.0, v134
	v_exp_f32_e32 v179, v28
	v_cvt_pk_f32_fp8_sdwa v[28:29], v183 src0_sel:WORD_1
	v_med3_f32 v30, v30, s35, v177
	v_med3_f32 v31, v31, s35, v177
	v_med3_f32 v28, v28, s35, v177
	v_mul_f32_e32 v30, 0xbfb8aa3b, v30
	v_mul_f32_e32 v31, 0xbfb8aa3b, v31
	v_med3_f32 v32, v32, s35, v177
	v_med3_f32 v33, v33, s35, v177
	v_mul_f32_e32 v28, 0xbfb8aa3b, v28
	v_med3_f32 v29, v29, s35, v177
	v_exp_f32_e32 v30, v30
	v_exp_f32_e32 v31, v31
	v_mul_f32_e32 v32, 0xbfb8aa3b, v32
	v_mul_f32_e32 v33, 0xbfb8aa3b, v33
	v_exp_f32_e32 v28, v28
	v_mul_f32_e32 v29, 0xbfb8aa3b, v29
	v_exp_f32_e32 v32, v32
	v_exp_f32_e32 v33, v33
	v_exp_f32_e32 v29, v29
	v_rcp_f32_e32 v178, v134
	v_add_f32_e32 v134, 1.0, v179
	v_add_f32_e32 v30, 1.0, v30
	v_add_f32_e32 v31, 1.0, v31
	v_add_f32_e32 v28, 1.0, v28
	v_rcp_f32_e32 v179, v134
	v_rcp_f32_e32 v30, v30
	v_rcp_f32_e32 v31, v31
	v_add_f32_e32 v32, 1.0, v32
	v_add_f32_e32 v33, 1.0, v33
	v_rcp_f32_e32 v180, v28
	v_add_f32_e32 v28, 1.0, v29
	v_rcp_f32_e32 v32, v32
	v_rcp_f32_e32 v33, v33
	v_rcp_f32_e32 v181, v28
	v_pk_mul_f32 v[28:29], v[38:39], v[178:179]
	v_pk_mul_f32 v[30:31], v[40:41], v[30:31]
	v_cvt_pk_bf16_f32 v28, v28, v29
	v_cvt_pk_bf16_f32 v29, v30, v31
	v_pk_mul_f32 v[30:31], v[42:43], v[32:33]
	v_pk_mul_f32 v[32:33], v[44:45], v[180:181]
	v_cvt_pk_bf16_f32 v30, v30, v31
	v_cvt_pk_bf16_f32 v31, v32, v33
	global_store_dwordx4 v[26:27], v[28:31], off offset:256
	s_waitcnt vmcnt(15)
	v_cvt_pk_f32_fp8_e32 v[32:33], v162
	v_cvt_pk_f32_fp8_sdwa v[28:29], v162 src0_sel:WORD_1
	v_cvt_pk_f32_fp8_e32 v[30:31], v163
	v_med3_f32 v32, v32, s35, v177
	v_mul_f32_e32 v32, 0xbfb8aa3b, v32
	v_med3_f32 v28, v28, s35, v177
	v_mul_f32_e32 v28, 0xbfb8aa3b, v28
	v_med3_f32 v29, v29, s35, v177
	v_exp_f32_e32 v28, v28
	v_mul_f32_e32 v29, 0xbfb8aa3b, v29
	v_exp_f32_e32 v29, v29
	v_exp_f32_e32 v38, v32
	v_add_f32_e32 v28, 1.0, v28
	v_rcp_f32_e32 v40, v28
	v_add_f32_e32 v28, 1.0, v29
	v_med3_f32 v32, v33, s35, v177
	v_med3_f32 v29, v30, s35, v177
	v_mul_f32_e32 v32, 0xbfb8aa3b, v32
	v_mul_f32_e32 v29, 0xbfb8aa3b, v29
	v_med3_f32 v30, v31, s35, v177
	v_exp_f32_e32 v39, v32
	v_cvt_pk_f32_fp8_sdwa v[32:33], v163 src0_sel:WORD_1
	v_exp_f32_e32 v29, v29
	v_mul_f32_e32 v30, 0xbfb8aa3b, v30
	v_exp_f32_e32 v31, v30
	v_rcp_f32_e32 v41, v28
	v_add_f32_e32 v28, 1.0, v29
	v_rcp_f32_e32 v30, v28
	v_add_f32_e32 v28, 1.0, v31
	v_med3_f32 v29, v32, s35, v177
	v_mul_f32_e32 v29, 0xbfb8aa3b, v29
	v_med3_f32 v31, v33, s35, v177
	v_exp_f32_e32 v29, v29
	v_mul_f32_e32 v31, 0xbfb8aa3b, v31
	v_exp_f32_e32 v33, v31
	v_rcp_f32_e32 v31, v28
	v_add_f32_e32 v28, 1.0, v29
	v_rcp_f32_e32 v32, v28
	v_add_f32_e32 v28, 1.0, v33
	v_add_f32_e32 v38, 1.0, v38
	v_add_f32_e32 v39, 1.0, v39
	v_rcp_f32_e32 v33, v28
	v_rcp_f32_e32 v38, v38
	v_rcp_f32_e32 v39, v39
	v_pk_mul_f32 v[30:31], v[54:55], v[30:31]
	v_pk_mul_f32 v[32:33], v[56:57], v[32:33]
	v_cvt_pk_bf16_f32 v30, v30, v31
	v_pk_mul_f32 v[28:29], v[50:51], v[38:39]
	v_pk_mul_f32 v[38:39], v[52:53], v[40:41]
	v_cvt_pk_bf16_f32 v31, v32, v33
	v_add_co_u32_e32 v32, vcc, s2, v26
	v_cvt_pk_bf16_f32 v28, v28, v29
	v_cvt_pk_bf16_f32 v29, v38, v39
	v_addc_co_u32_e32 v33, vcc, 0, v27, vcc
	global_store_dwordx4 v[32:33], v[28:31], off
	s_waitcnt vmcnt(15)
	v_cvt_pk_f32_fp8_e32 v[38:39], v160
	s_mov_b32 s2, 0x10000
	v_cvt_pk_f32_fp8_sdwa v[28:29], v160 src0_sel:WORD_1
	v_cvt_pk_f32_fp8_e32 v[30:31], v161
	v_med3_f32 v38, v38, s35, v177
	v_med3_f32 v28, v28, s35, v177
	v_mul_f32_e32 v28, 0xbfb8aa3b, v28
	v_med3_f32 v29, v29, s35, v177
	v_exp_f32_e32 v28, v28
	v_mul_f32_e32 v29, 0xbfb8aa3b, v29
	v_exp_f32_e32 v29, v29
	v_mul_f32_e32 v38, 0xbfb8aa3b, v38
	v_add_f32_e32 v28, 1.0, v28
	v_exp_f32_e32 v40, v38
	v_rcp_f32_e32 v42, v28
	v_add_f32_e32 v28, 1.0, v29
	v_med3_f32 v38, v39, s35, v177
	v_med3_f32 v29, v30, s35, v177
	v_mul_f32_e32 v38, 0xbfb8aa3b, v38
	v_mul_f32_e32 v29, 0xbfb8aa3b, v29
	v_med3_f32 v30, v31, s35, v177
	v_exp_f32_e32 v41, v38
	v_cvt_pk_f32_fp8_sdwa v[38:39], v161 src0_sel:WORD_1
	v_exp_f32_e32 v29, v29
	v_mul_f32_e32 v30, 0xbfb8aa3b, v30
	v_exp_f32_e32 v31, v30
	v_rcp_f32_e32 v43, v28
	v_add_f32_e32 v28, 1.0, v29
	v_rcp_f32_e32 v30, v28
	v_add_f32_e32 v28, 1.0, v31
	v_med3_f32 v29, v38, s35, v177
	v_mul_f32_e32 v29, 0xbfb8aa3b, v29
	v_med3_f32 v31, v39, s35, v177
	v_exp_f32_e32 v29, v29
	v_mul_f32_e32 v31, 0xbfb8aa3b, v31
	v_exp_f32_e32 v39, v31
	v_rcp_f32_e32 v31, v28
	v_add_f32_e32 v28, 1.0, v29
	v_add_f32_e32 v40, 1.0, v40
	v_add_f32_e32 v41, 1.0, v41
	v_rcp_f32_e32 v38, v28
	v_add_f32_e32 v28, 1.0, v39
	v_rcp_f32_e32 v40, v40
	v_rcp_f32_e32 v41, v41
	v_rcp_f32_e32 v39, v28
	v_pk_mul_f32 v[30:31], v[66:67], v[30:31]
	v_pk_mul_f32 v[28:29], v[62:63], v[40:41]
	v_pk_mul_f32 v[40:41], v[64:65], v[42:43]
	v_pk_mul_f32 v[38:39], v[68:69], v[38:39]
	v_cvt_pk_bf16_f32 v28, v28, v29
	v_cvt_pk_bf16_f32 v29, v40, v41
	v_cvt_pk_bf16_f32 v30, v30, v31
	v_cvt_pk_bf16_f32 v31, v38, v39
	global_store_dwordx4 v[32:33], v[28:31], off offset:256
	s_waitcnt vmcnt(15)
	v_cvt_pk_f32_fp8_e32 v[38:39], v158
	v_cvt_pk_f32_fp8_sdwa v[28:29], v158 src0_sel:WORD_1
	v_cvt_pk_f32_fp8_e32 v[30:31], v159
	v_med3_f32 v32, v38, s35, v177
	v_mul_f32_e32 v32, 0xbfb8aa3b, v32
	v_med3_f32 v28, v28, s35, v177
	v_mul_f32_e32 v28, 0xbfb8aa3b, v28
	v_med3_f32 v29, v29, s35, v177
	v_exp_f32_e32 v28, v28
	v_mul_f32_e32 v29, 0xbfb8aa3b, v29
	v_exp_f32_e32 v29, v29
	v_exp_f32_e32 v38, v32
	v_add_f32_e32 v28, 1.0, v28
	v_rcp_f32_e32 v40, v28
	v_add_f32_e32 v28, 1.0, v29
	v_med3_f32 v32, v39, s35, v177
	v_med3_f32 v29, v30, s35, v177
	v_mul_f32_e32 v32, 0xbfb8aa3b, v32
	v_mul_f32_e32 v29, 0xbfb8aa3b, v29
	v_med3_f32 v30, v31, s35, v177
	v_exp_f32_e32 v39, v32
	v_cvt_pk_f32_fp8_sdwa v[32:33], v159 src0_sel:WORD_1
	v_exp_f32_e32 v29, v29
	v_mul_f32_e32 v30, 0xbfb8aa3b, v30
	v_exp_f32_e32 v31, v30
	v_rcp_f32_e32 v41, v28
	v_add_f32_e32 v28, 1.0, v29
	v_rcp_f32_e32 v30, v28
	v_add_f32_e32 v28, 1.0, v31
	v_med3_f32 v29, v32, s35, v177
	v_mul_f32_e32 v29, 0xbfb8aa3b, v29
	v_med3_f32 v31, v33, s35, v177
	v_exp_f32_e32 v29, v29
	v_mul_f32_e32 v31, 0xbfb8aa3b, v31
	v_exp_f32_e32 v33, v31
	v_rcp_f32_e32 v31, v28
	v_add_f32_e32 v28, 1.0, v29
	v_rcp_f32_e32 v32, v28
	v_add_f32_e32 v28, 1.0, v33
	v_add_f32_e32 v38, 1.0, v38
	v_add_f32_e32 v39, 1.0, v39
	v_rcp_f32_e32 v33, v28
	v_rcp_f32_e32 v38, v38
	v_rcp_f32_e32 v39, v39
	v_pk_mul_f32 v[30:31], v[78:79], v[30:31]
	v_pk_mul_f32 v[32:33], v[80:81], v[32:33]
	v_cvt_pk_bf16_f32 v30, v30, v31
	v_pk_mul_f32 v[28:29], v[74:75], v[38:39]
	v_pk_mul_f32 v[38:39], v[76:77], v[40:41]
	v_cvt_pk_bf16_f32 v31, v32, v33
	v_add_co_u32_e32 v32, vcc, s2, v26
	v_cvt_pk_bf16_f32 v28, v28, v29
	v_cvt_pk_bf16_f32 v29, v38, v39
	v_addc_co_u32_e32 v33, vcc, 0, v27, vcc
	global_store_dwordx4 v[32:33], v[28:31], off
	s_waitcnt vmcnt(15)
	v_cvt_pk_f32_fp8_e32 v[38:39], v156
	s_mov_b32 s2, 0x18000
	v_cvt_pk_f32_fp8_sdwa v[28:29], v156 src0_sel:WORD_1
	v_cvt_pk_f32_fp8_e32 v[30:31], v157
	v_med3_f32 v38, v38, s35, v177
	v_med3_f32 v28, v28, s35, v177
	v_mul_f32_e32 v28, 0xbfb8aa3b, v28
	v_med3_f32 v29, v29, s35, v177
	v_exp_f32_e32 v28, v28
	v_mul_f32_e32 v29, 0xbfb8aa3b, v29
	v_exp_f32_e32 v29, v29
	v_mul_f32_e32 v38, 0xbfb8aa3b, v38
	v_add_f32_e32 v28, 1.0, v28
	v_exp_f32_e32 v40, v38
	v_rcp_f32_e32 v42, v28
	v_add_f32_e32 v28, 1.0, v29
	v_med3_f32 v38, v39, s35, v177
	v_med3_f32 v29, v30, s35, v177
	v_mul_f32_e32 v38, 0xbfb8aa3b, v38
	v_mul_f32_e32 v29, 0xbfb8aa3b, v29
	v_med3_f32 v30, v31, s35, v177
	v_exp_f32_e32 v41, v38
	v_cvt_pk_f32_fp8_sdwa v[38:39], v157 src0_sel:WORD_1
	v_exp_f32_e32 v29, v29
	v_mul_f32_e32 v30, 0xbfb8aa3b, v30
	v_exp_f32_e32 v31, v30
	v_rcp_f32_e32 v43, v28
	v_add_f32_e32 v28, 1.0, v29
	v_rcp_f32_e32 v30, v28
	v_add_f32_e32 v28, 1.0, v31
	v_med3_f32 v29, v38, s35, v177
	v_mul_f32_e32 v29, 0xbfb8aa3b, v29
	v_med3_f32 v31, v39, s35, v177
	v_exp_f32_e32 v29, v29
	v_mul_f32_e32 v31, 0xbfb8aa3b, v31
	v_exp_f32_e32 v39, v31
	v_rcp_f32_e32 v31, v28
	v_add_f32_e32 v28, 1.0, v29
	v_add_f32_e32 v40, 1.0, v40
	v_add_f32_e32 v41, 1.0, v41
	v_rcp_f32_e32 v38, v28
	v_add_f32_e32 v28, 1.0, v39
	v_rcp_f32_e32 v40, v40
	v_rcp_f32_e32 v41, v41
	v_rcp_f32_e32 v39, v28
	v_pk_mul_f32 v[30:31], v[90:91], v[30:31]
	v_pk_mul_f32 v[28:29], v[82:83], v[40:41]
	v_pk_mul_f32 v[40:41], v[84:85], v[42:43]
	v_pk_mul_f32 v[38:39], v[92:93], v[38:39]
	v_cvt_pk_bf16_f32 v28, v28, v29
	v_cvt_pk_bf16_f32 v29, v40, v41
	v_cvt_pk_bf16_f32 v30, v30, v31
	v_cvt_pk_bf16_f32 v31, v38, v39
	global_store_dwordx4 v[32:33], v[28:31], off offset:256
	s_waitcnt vmcnt(15)
	v_cvt_pk_f32_fp8_e32 v[38:39], v154
	v_cvt_pk_f32_fp8_sdwa v[28:29], v154 src0_sel:WORD_1
	v_cvt_pk_f32_fp8_e32 v[30:31], v155
	v_med3_f32 v32, v38, s35, v177
	v_mul_f32_e32 v32, 0xbfb8aa3b, v32
	v_med3_f32 v28, v28, s35, v177
	v_mul_f32_e32 v28, 0xbfb8aa3b, v28
	v_med3_f32 v29, v29, s35, v177
	v_exp_f32_e32 v28, v28
	v_mul_f32_e32 v29, 0xbfb8aa3b, v29
	v_exp_f32_e32 v29, v29
	v_exp_f32_e32 v38, v32
	v_add_f32_e32 v28, 1.0, v28
	v_rcp_f32_e32 v40, v28
	v_add_f32_e32 v28, 1.0, v29
	v_med3_f32 v32, v39, s35, v177
	v_med3_f32 v29, v30, s35, v177
	v_mul_f32_e32 v32, 0xbfb8aa3b, v32
	v_mul_f32_e32 v29, 0xbfb8aa3b, v29
	v_med3_f32 v30, v31, s35, v177
	v_exp_f32_e32 v39, v32
	v_cvt_pk_f32_fp8_sdwa v[32:33], v155 src0_sel:WORD_1
	v_exp_f32_e32 v29, v29
	v_mul_f32_e32 v30, 0xbfb8aa3b, v30
	v_exp_f32_e32 v31, v30
	v_rcp_f32_e32 v41, v28
	v_add_f32_e32 v28, 1.0, v29
	v_rcp_f32_e32 v30, v28
	v_add_f32_e32 v28, 1.0, v31
	v_med3_f32 v29, v32, s35, v177
	v_mul_f32_e32 v29, 0xbfb8aa3b, v29
	v_med3_f32 v31, v33, s35, v177
	v_exp_f32_e32 v29, v29
	v_mul_f32_e32 v31, 0xbfb8aa3b, v31
	v_exp_f32_e32 v33, v31
	v_rcp_f32_e32 v31, v28
	v_add_f32_e32 v28, 1.0, v29
	v_rcp_f32_e32 v32, v28
	v_add_f32_e32 v28, 1.0, v33
	v_add_f32_e32 v38, 1.0, v38
	v_add_f32_e32 v39, 1.0, v39
	v_rcp_f32_e32 v33, v28
	v_rcp_f32_e32 v38, v38
	v_rcp_f32_e32 v39, v39
	v_pk_mul_f32 v[30:31], v[102:103], v[30:31]
	v_pk_mul_f32 v[32:33], v[104:105], v[32:33]
	v_cvt_pk_bf16_f32 v30, v30, v31
	v_pk_mul_f32 v[28:29], v[94:95], v[38:39]
	v_pk_mul_f32 v[38:39], v[96:97], v[40:41]
	v_cvt_pk_bf16_f32 v31, v32, v33
	v_add_co_u32_e32 v32, vcc, s2, v26
	v_cvt_pk_bf16_f32 v28, v28, v29
	v_cvt_pk_bf16_f32 v29, v38, v39
	v_addc_co_u32_e32 v33, vcc, 0, v27, vcc
	global_store_dwordx4 v[32:33], v[28:31], off
	s_waitcnt vmcnt(15)
	v_cvt_pk_f32_fp8_e32 v[38:39], v152
	s_mov_b32 s2, 0x40000
	v_cvt_pk_f32_fp8_sdwa v[28:29], v152 src0_sel:WORD_1
	v_cvt_pk_f32_fp8_e32 v[30:31], v153
	v_med3_f32 v38, v38, s35, v177
	v_med3_f32 v28, v28, s35, v177
	v_mul_f32_e32 v28, 0xbfb8aa3b, v28
	v_med3_f32 v29, v29, s35, v177
	v_exp_f32_e32 v28, v28
	v_mul_f32_e32 v29, 0xbfb8aa3b, v29
	v_exp_f32_e32 v29, v29
	v_mul_f32_e32 v38, 0xbfb8aa3b, v38
	v_add_f32_e32 v28, 1.0, v28
	v_exp_f32_e32 v40, v38
	v_rcp_f32_e32 v42, v28
	v_add_f32_e32 v28, 1.0, v29
	v_med3_f32 v38, v39, s35, v177
	v_med3_f32 v29, v30, s35, v177
	v_mul_f32_e32 v38, 0xbfb8aa3b, v38
	v_mul_f32_e32 v29, 0xbfb8aa3b, v29
	v_med3_f32 v30, v31, s35, v177
	v_exp_f32_e32 v41, v38
	v_cvt_pk_f32_fp8_sdwa v[38:39], v153 src0_sel:WORD_1
	v_exp_f32_e32 v29, v29
	v_mul_f32_e32 v30, 0xbfb8aa3b, v30
	v_exp_f32_e32 v31, v30
	v_rcp_f32_e32 v43, v28
	v_add_f32_e32 v28, 1.0, v29
	v_rcp_f32_e32 v30, v28
	v_add_f32_e32 v28, 1.0, v31
	v_med3_f32 v29, v38, s35, v177
	v_mul_f32_e32 v29, 0xbfb8aa3b, v29
	v_med3_f32 v31, v39, s35, v177
	v_exp_f32_e32 v29, v29
	v_mul_f32_e32 v31, 0xbfb8aa3b, v31
	v_exp_f32_e32 v39, v31
	v_rcp_f32_e32 v31, v28
	v_add_f32_e32 v28, 1.0, v29
	v_add_f32_e32 v40, 1.0, v40
	v_add_f32_e32 v41, 1.0, v41
	v_rcp_f32_e32 v38, v28
	v_add_f32_e32 v28, 1.0, v39
	v_rcp_f32_e32 v40, v40
	v_rcp_f32_e32 v41, v41
	v_rcp_f32_e32 v39, v28
	v_pk_mul_f32 v[30:31], v[114:115], v[30:31]
	v_pk_mul_f32 v[28:29], v[106:107], v[40:41]
	v_pk_mul_f32 v[40:41], v[108:109], v[42:43]
	v_pk_mul_f32 v[38:39], v[116:117], v[38:39]
	v_cvt_pk_bf16_f32 v28, v28, v29
	v_cvt_pk_bf16_f32 v29, v40, v41
	v_cvt_pk_bf16_f32 v30, v30, v31
	v_cvt_pk_bf16_f32 v31, v38, v39
	global_store_dwordx4 v[32:33], v[28:31], off offset:256
	s_waitcnt vmcnt(15)
	v_cvt_pk_f32_fp8_e32 v[38:39], v150
	v_cvt_pk_f32_fp8_sdwa v[28:29], v150 src0_sel:WORD_1
	v_cvt_pk_f32_fp8_e32 v[30:31], v151
	v_med3_f32 v32, v38, s35, v177
	v_mul_f32_e32 v32, 0xbfb8aa3b, v32
	v_med3_f32 v28, v28, s35, v177
	v_mul_f32_e32 v28, 0xbfb8aa3b, v28
	v_med3_f32 v29, v29, s35, v177
	v_exp_f32_e32 v28, v28
	v_mul_f32_e32 v29, 0xbfb8aa3b, v29
	v_exp_f32_e32 v29, v29
	v_exp_f32_e32 v38, v32
	v_add_f32_e32 v28, 1.0, v28
	v_rcp_f32_e32 v40, v28
	v_add_f32_e32 v28, 1.0, v29
	v_med3_f32 v32, v39, s35, v177
	v_med3_f32 v29, v30, s35, v177
	v_mul_f32_e32 v32, 0xbfb8aa3b, v32
	v_mul_f32_e32 v29, 0xbfb8aa3b, v29
	v_med3_f32 v30, v31, s35, v177
	v_exp_f32_e32 v39, v32
	v_cvt_pk_f32_fp8_sdwa v[32:33], v151 src0_sel:WORD_1
	v_exp_f32_e32 v29, v29
	v_mul_f32_e32 v30, 0xbfb8aa3b, v30
	v_exp_f32_e32 v31, v30
	v_rcp_f32_e32 v41, v28
	v_add_f32_e32 v28, 1.0, v29
	v_rcp_f32_e32 v30, v28
	v_add_f32_e32 v28, 1.0, v31
	v_med3_f32 v29, v32, s35, v177
	v_mul_f32_e32 v29, 0xbfb8aa3b, v29
	v_med3_f32 v31, v33, s35, v177
	v_exp_f32_e32 v29, v29
	v_mul_f32_e32 v31, 0xbfb8aa3b, v31
	v_exp_f32_e32 v33, v31
	v_rcp_f32_e32 v31, v28
	v_add_f32_e32 v28, 1.0, v29
	v_rcp_f32_e32 v32, v28
	v_add_f32_e32 v28, 1.0, v33
	v_add_f32_e32 v38, 1.0, v38
	v_add_f32_e32 v39, 1.0, v39
	v_rcp_f32_e32 v33, v28
	v_rcp_f32_e32 v38, v38
	v_rcp_f32_e32 v39, v39
	v_pk_mul_f32 v[30:31], v[126:127], v[30:31]
	v_pk_mul_f32 v[32:33], v[128:129], v[32:33]
	v_cvt_pk_bf16_f32 v30, v30, v31
	v_pk_mul_f32 v[28:29], v[118:119], v[38:39]
	v_pk_mul_f32 v[38:39], v[120:121], v[40:41]
	v_cvt_pk_bf16_f32 v31, v32, v33
	v_add_co_u32_e32 v32, vcc, s2, v26
	v_cvt_pk_bf16_f32 v28, v28, v29
	v_cvt_pk_bf16_f32 v29, v38, v39
	v_addc_co_u32_e32 v33, vcc, 0, v27, vcc
	global_store_dwordx4 v[32:33], v[28:31], off
	s_waitcnt vmcnt(15)
	v_cvt_pk_f32_fp8_e32 v[38:39], v148
	s_mov_b32 s2, 0x48000
	v_cvt_pk_f32_fp8_sdwa v[28:29], v148 src0_sel:WORD_1
	v_cvt_pk_f32_fp8_e32 v[30:31], v149
	v_med3_f32 v38, v38, s35, v177
	v_med3_f32 v28, v28, s35, v177
	v_mul_f32_e32 v28, 0xbfb8aa3b, v28
	v_med3_f32 v29, v29, s35, v177
	v_exp_f32_e32 v28, v28
	v_mul_f32_e32 v29, 0xbfb8aa3b, v29
	v_exp_f32_e32 v29, v29
	v_mul_f32_e32 v38, 0xbfb8aa3b, v38
	v_add_f32_e32 v28, 1.0, v28
	v_exp_f32_e32 v40, v38
	v_rcp_f32_e32 v42, v28
	v_add_f32_e32 v28, 1.0, v29
	v_med3_f32 v38, v39, s35, v177
	v_med3_f32 v29, v30, s35, v177
	v_mul_f32_e32 v38, 0xbfb8aa3b, v38
	v_mul_f32_e32 v29, 0xbfb8aa3b, v29
	v_med3_f32 v30, v31, s35, v177
	v_exp_f32_e32 v41, v38
	v_cvt_pk_f32_fp8_sdwa v[38:39], v149 src0_sel:WORD_1
	v_exp_f32_e32 v29, v29
	v_mul_f32_e32 v30, 0xbfb8aa3b, v30
	v_exp_f32_e32 v31, v30
	v_rcp_f32_e32 v43, v28
	v_add_f32_e32 v28, 1.0, v29
	v_rcp_f32_e32 v30, v28
	v_add_f32_e32 v28, 1.0, v31
	v_med3_f32 v29, v38, s35, v177
	v_mul_f32_e32 v29, 0xbfb8aa3b, v29
	v_med3_f32 v31, v39, s35, v177
	v_exp_f32_e32 v29, v29
	v_mul_f32_e32 v31, 0xbfb8aa3b, v31
	v_exp_f32_e32 v39, v31
	v_rcp_f32_e32 v31, v28
	v_add_f32_e32 v28, 1.0, v29
	v_add_f32_e32 v40, 1.0, v40
	v_add_f32_e32 v41, 1.0, v41
	v_rcp_f32_e32 v38, v28
	v_add_f32_e32 v28, 1.0, v39
	v_rcp_f32_e32 v40, v40
	v_rcp_f32_e32 v41, v41
	v_rcp_f32_e32 v39, v28
	v_pk_mul_f32 v[30:31], v[110:111], v[30:31]
	v_pk_mul_f32 v[28:29], v[122:123], v[40:41]
	v_pk_mul_f32 v[40:41], v[124:125], v[42:43]
	v_pk_mul_f32 v[38:39], v[112:113], v[38:39]
	v_cvt_pk_bf16_f32 v28, v28, v29
	v_cvt_pk_bf16_f32 v29, v40, v41
	v_cvt_pk_bf16_f32 v30, v30, v31
	v_cvt_pk_bf16_f32 v31, v38, v39
	global_store_dwordx4 v[32:33], v[28:31], off offset:256
	s_waitcnt vmcnt(15)
	v_cvt_pk_f32_fp8_e32 v[38:39], v146
	v_cvt_pk_f32_fp8_sdwa v[28:29], v146 src0_sel:WORD_1
	v_cvt_pk_f32_fp8_e32 v[30:31], v147
	v_med3_f32 v32, v38, s35, v177
	v_mul_f32_e32 v32, 0xbfb8aa3b, v32
	v_med3_f32 v28, v28, s35, v177
	v_mul_f32_e32 v28, 0xbfb8aa3b, v28
	v_med3_f32 v29, v29, s35, v177
	v_exp_f32_e32 v28, v28
	v_mul_f32_e32 v29, 0xbfb8aa3b, v29
	v_exp_f32_e32 v29, v29
	v_exp_f32_e32 v38, v32
	v_add_f32_e32 v28, 1.0, v28
	v_rcp_f32_e32 v40, v28
	v_add_f32_e32 v28, 1.0, v29
	v_med3_f32 v32, v39, s35, v177
	v_med3_f32 v29, v30, s35, v177
	v_mul_f32_e32 v32, 0xbfb8aa3b, v32
	v_mul_f32_e32 v29, 0xbfb8aa3b, v29
	v_med3_f32 v30, v31, s35, v177
	v_exp_f32_e32 v39, v32
	v_cvt_pk_f32_fp8_sdwa v[32:33], v147 src0_sel:WORD_1
	v_exp_f32_e32 v29, v29
	v_mul_f32_e32 v30, 0xbfb8aa3b, v30
	v_exp_f32_e32 v31, v30
	v_rcp_f32_e32 v41, v28
	v_add_f32_e32 v28, 1.0, v29
	v_rcp_f32_e32 v30, v28
	v_add_f32_e32 v28, 1.0, v31
	v_med3_f32 v29, v32, s35, v177
	v_mul_f32_e32 v29, 0xbfb8aa3b, v29
	v_med3_f32 v31, v33, s35, v177
	v_exp_f32_e32 v29, v29
	v_mul_f32_e32 v31, 0xbfb8aa3b, v31
	v_exp_f32_e32 v33, v31
	v_rcp_f32_e32 v31, v28
	v_add_f32_e32 v28, 1.0, v29
	v_rcp_f32_e32 v32, v28
	v_add_f32_e32 v28, 1.0, v33
	v_add_f32_e32 v38, 1.0, v38
	v_add_f32_e32 v39, 1.0, v39
	v_rcp_f32_e32 v33, v28
	v_rcp_f32_e32 v38, v38
	v_rcp_f32_e32 v39, v39
	v_pk_mul_f32 v[30:31], v[86:87], v[30:31]
	v_pk_mul_f32 v[32:33], v[88:89], v[32:33]
	v_cvt_pk_bf16_f32 v30, v30, v31
	v_pk_mul_f32 v[28:29], v[98:99], v[38:39]
	v_pk_mul_f32 v[38:39], v[100:101], v[40:41]
	v_cvt_pk_bf16_f32 v31, v32, v33
	v_add_co_u32_e32 v32, vcc, s2, v26
	v_cvt_pk_bf16_f32 v28, v28, v29
	v_cvt_pk_bf16_f32 v29, v38, v39
	v_addc_co_u32_e32 v33, vcc, 0, v27, vcc
	global_store_dwordx4 v[32:33], v[28:31], off
	s_waitcnt vmcnt(15)
	v_cvt_pk_f32_fp8_e32 v[38:39], v144
	s_mov_b32 s2, 0x50000
	v_cvt_pk_f32_fp8_sdwa v[28:29], v144 src0_sel:WORD_1
	v_cvt_pk_f32_fp8_e32 v[30:31], v145
	v_med3_f32 v38, v38, s35, v177
	v_med3_f32 v28, v28, s35, v177
	v_mul_f32_e32 v28, 0xbfb8aa3b, v28
	v_med3_f32 v29, v29, s35, v177
	v_exp_f32_e32 v28, v28
	v_mul_f32_e32 v29, 0xbfb8aa3b, v29
	v_exp_f32_e32 v29, v29
	v_mul_f32_e32 v38, 0xbfb8aa3b, v38
	v_add_f32_e32 v28, 1.0, v28
	v_exp_f32_e32 v40, v38
	v_rcp_f32_e32 v42, v28
	v_add_f32_e32 v28, 1.0, v29
	v_med3_f32 v38, v39, s35, v177
	v_med3_f32 v29, v30, s35, v177
	v_mul_f32_e32 v38, 0xbfb8aa3b, v38
	v_mul_f32_e32 v29, 0xbfb8aa3b, v29
	v_med3_f32 v30, v31, s35, v177
	v_exp_f32_e32 v41, v38
	v_cvt_pk_f32_fp8_sdwa v[38:39], v145 src0_sel:WORD_1
	v_exp_f32_e32 v29, v29
	v_mul_f32_e32 v30, 0xbfb8aa3b, v30
	v_exp_f32_e32 v31, v30
	v_rcp_f32_e32 v43, v28
	v_add_f32_e32 v28, 1.0, v29
	v_rcp_f32_e32 v30, v28
	v_add_f32_e32 v28, 1.0, v31
	v_med3_f32 v29, v38, s35, v177
	v_mul_f32_e32 v29, 0xbfb8aa3b, v29
	v_med3_f32 v31, v39, s35, v177
	v_exp_f32_e32 v29, v29
	v_mul_f32_e32 v31, 0xbfb8aa3b, v31
	v_exp_f32_e32 v39, v31
	v_rcp_f32_e32 v31, v28
	v_add_f32_e32 v28, 1.0, v29
	v_add_f32_e32 v40, 1.0, v40
	v_add_f32_e32 v41, 1.0, v41
	v_rcp_f32_e32 v38, v28
	v_add_f32_e32 v28, 1.0, v39
	v_rcp_f32_e32 v40, v40
	v_rcp_f32_e32 v41, v41
	v_rcp_f32_e32 v39, v28
	v_pk_mul_f32 v[30:31], v[58:59], v[30:31]
	v_pk_mul_f32 v[28:29], v[70:71], v[40:41]
	v_pk_mul_f32 v[40:41], v[72:73], v[42:43]
	v_pk_mul_f32 v[38:39], v[60:61], v[38:39]
	v_cvt_pk_bf16_f32 v28, v28, v29
	v_cvt_pk_bf16_f32 v29, v40, v41
	v_cvt_pk_bf16_f32 v30, v30, v31
	v_cvt_pk_bf16_f32 v31, v38, v39
	global_store_dwordx4 v[32:33], v[28:31], off offset:256
	s_waitcnt vmcnt(15)
	v_cvt_pk_f32_fp8_e32 v[38:39], v142
	v_cvt_pk_f32_fp8_sdwa v[28:29], v142 src0_sel:WORD_1
	v_cvt_pk_f32_fp8_e32 v[30:31], v143
	v_med3_f32 v32, v38, s35, v177
	v_mul_f32_e32 v32, 0xbfb8aa3b, v32
	v_med3_f32 v28, v28, s35, v177
	v_mul_f32_e32 v28, 0xbfb8aa3b, v28
	v_med3_f32 v29, v29, s35, v177
	v_exp_f32_e32 v28, v28
	v_mul_f32_e32 v29, 0xbfb8aa3b, v29
	v_exp_f32_e32 v29, v29
	v_exp_f32_e32 v38, v32
	v_add_f32_e32 v28, 1.0, v28
	v_rcp_f32_e32 v40, v28
	v_add_f32_e32 v28, 1.0, v29
	v_med3_f32 v29, v30, s35, v177
	v_med3_f32 v32, v39, s35, v177
	v_mul_f32_e32 v29, 0xbfb8aa3b, v29
	v_med3_f32 v30, v31, s35, v177
	v_mul_f32_e32 v32, 0xbfb8aa3b, v32
	v_exp_f32_e32 v29, v29
	v_mul_f32_e32 v30, 0xbfb8aa3b, v30
	v_exp_f32_e32 v39, v32
	v_cvt_pk_f32_fp8_sdwa v[32:33], v143 src0_sel:WORD_1
	v_exp_f32_e32 v31, v30
	v_rcp_f32_e32 v41, v28
	v_add_f32_e32 v28, 1.0, v29
	v_rcp_f32_e32 v30, v28
	v_add_f32_e32 v28, 1.0, v31
	v_med3_f32 v29, v32, s35, v177
	v_med3_f32 v31, v33, s35, v177
	v_mul_f32_e32 v29, 0xbfb8aa3b, v29
	v_mul_f32_e32 v31, 0xbfb8aa3b, v31
	v_exp_f32_e32 v29, v29
	v_exp_f32_e32 v33, v31
	v_rcp_f32_e32 v31, v28
	v_add_f32_e32 v38, 1.0, v38
	v_add_f32_e32 v28, 1.0, v29
	v_rcp_f32_e32 v32, v28
	v_pk_mul_f32 v[30:31], v[34:35], v[30:31]
	s_waitcnt vmcnt(14)
	v_cvt_pk_f32_fp8_e32 v[34:35], v140
	v_add_f32_e32 v28, 1.0, v33
	v_add_f32_e32 v39, 1.0, v39
	v_rcp_f32_e32 v33, v28
	v_rcp_f32_e32 v38, v38
	v_rcp_f32_e32 v39, v39
	v_med3_f32 v34, v34, s35, v177
	v_pk_mul_f32 v[32:33], v[36:37], v[32:33]
	v_mul_f32_e32 v34, 0xbfb8aa3b, v34
	v_pk_mul_f32 v[28:29], v[46:47], v[38:39]
	v_pk_mul_f32 v[38:39], v[48:49], v[40:41]
	v_cvt_pk_bf16_f32 v30, v30, v31
	v_cvt_pk_bf16_f32 v31, v32, v33
	v_add_co_u32_e32 v32, vcc, s2, v26
	v_exp_f32_e32 v36, v34
	v_cvt_pk_bf16_f32 v28, v28, v29
	v_cvt_pk_bf16_f32 v29, v38, v39
	v_addc_co_u32_e32 v33, vcc, 0, v27, vcc
	v_med3_f32 v34, v35, s35, v177
	global_store_dwordx4 v[32:33], v[28:31], off
	v_mul_f32_e32 v34, 0xbfb8aa3b, v34
	v_exp_f32_e32 v37, v34
	v_cvt_pk_f32_fp8_sdwa v[28:29], v140 src0_sel:WORD_1
	v_cvt_pk_f32_fp8_e32 v[30:31], v141
	v_cvt_pk_f32_fp8_sdwa v[34:35], v141 src0_sel:WORD_1
	v_add_f32_e32 v36, 1.0, v36
	v_med3_f32 v28, v28, s35, v177
	v_med3_f32 v29, v29, s35, v177
	v_med3_f32 v30, v30, s35, v177
	v_med3_f32 v31, v31, s35, v177
	v_mul_f32_e32 v28, 0xbfb8aa3b, v28
	v_mul_f32_e32 v29, 0xbfb8aa3b, v29
	v_mul_f32_e32 v30, 0xbfb8aa3b, v30
	v_mul_f32_e32 v31, 0xbfb8aa3b, v31
	v_med3_f32 v34, v34, s35, v177
	v_med3_f32 v35, v35, s35, v177
	v_exp_f32_e32 v28, v28
	v_exp_f32_e32 v29, v29
	v_exp_f32_e32 v30, v30
	v_exp_f32_e32 v31, v31
	v_mul_f32_e32 v34, 0xbfb8aa3b, v34
	v_mul_f32_e32 v35, 0xbfb8aa3b, v35
	v_exp_f32_e32 v34, v34
	v_exp_f32_e32 v35, v35
	v_add_f32_e32 v37, 1.0, v37
	v_add_f32_e32 v28, 1.0, v28
	v_add_f32_e32 v29, 1.0, v29
	v_add_f32_e32 v30, 1.0, v30
	v_add_f32_e32 v31, 1.0, v31
	v_rcp_f32_e32 v36, v36
	v_rcp_f32_e32 v37, v37
	v_rcp_f32_e32 v28, v28
	v_rcp_f32_e32 v29, v29
	v_rcp_f32_e32 v30, v30
	v_rcp_f32_e32 v31, v31
	v_add_f32_e32 v34, 1.0, v34
	v_add_f32_e32 v35, 1.0, v35
	v_rcp_f32_e32 v34, v34
	v_rcp_f32_e32 v35, v35
	v_pk_mul_f32 v[22:23], v[22:23], v[36:37]
	v_pk_mul_f32 v[24:25], v[24:25], v[28:29]
	v_pk_mul_f32 v[18:19], v[18:19], v[30:31]
	v_cvt_pk_bf16_f32 v22, v22, v23
	v_cvt_pk_bf16_f32 v23, v24, v25
	v_cvt_pk_bf16_f32 v24, v18, v19
	v_pk_mul_f32 v[18:19], v[20:21], v[34:35]
	s_waitcnt vmcnt(14)
	v_cvt_pk_f32_fp8_sdwa v[20:21], v138 src0_sel:WORD_1
	v_cvt_pk_bf16_f32 v25, v18, v19
	v_cvt_pk_f32_fp8_e32 v[18:19], v138
	global_store_dwordx4 v[32:33], v[22:25], off offset:256
	v_med3_f32 v18, v18, s35, v177
	v_mul_f32_e32 v18, 0xbfb8aa3b, v18
	v_exp_f32_e32 v24, v18
	v_med3_f32 v18, v19, s35, v177
	v_cvt_pk_f32_fp8_e32 v[22:23], v139
	v_mul_f32_e32 v18, 0xbfb8aa3b, v18
	v_exp_f32_e32 v25, v18
	v_cvt_pk_f32_fp8_sdwa v[18:19], v139 src0_sel:WORD_1
	v_med3_f32 v20, v20, s35, v177
	v_med3_f32 v21, v21, s35, v177
	v_med3_f32 v22, v22, s35, v177
	v_med3_f32 v23, v23, s35, v177
	v_mul_f32_e32 v20, 0xbfb8aa3b, v20
	v_mul_f32_e32 v21, 0xbfb8aa3b, v21
	v_mul_f32_e32 v22, 0xbfb8aa3b, v22
	v_mul_f32_e32 v23, 0xbfb8aa3b, v23
	v_med3_f32 v18, v18, s35, v177
	v_med3_f32 v19, v19, s35, v177
	v_exp_f32_e32 v20, v20
	v_exp_f32_e32 v21, v21
	v_exp_f32_e32 v22, v22
	v_exp_f32_e32 v23, v23
	v_mul_f32_e32 v18, 0xbfb8aa3b, v18
	v_mul_f32_e32 v19, 0xbfb8aa3b, v19
	v_exp_f32_e32 v18, v18
	v_exp_f32_e32 v19, v19
	v_add_f32_e32 v24, 1.0, v24
	v_add_f32_e32 v25, 1.0, v25
	v_add_f32_e32 v20, 1.0, v20
	v_add_f32_e32 v21, 1.0, v21
	v_add_f32_e32 v22, 1.0, v22
	v_add_f32_e32 v23, 1.0, v23
	v_rcp_f32_e32 v24, v24
	v_rcp_f32_e32 v25, v25
	v_rcp_f32_e32 v20, v20
	v_rcp_f32_e32 v21, v21
	v_rcp_f32_e32 v22, v22
	v_rcp_f32_e32 v23, v23
	v_add_f32_e32 v18, 1.0, v18
	v_add_f32_e32 v19, 1.0, v19
	v_rcp_f32_e32 v18, v18
	v_rcp_f32_e32 v19, v19
	v_pk_mul_f32 v[14:15], v[14:15], v[24:25]
	v_pk_mul_f32 v[16:17], v[16:17], v[20:21]
	v_pk_mul_f32 v[10:11], v[10:11], v[22:23]
	v_cvt_pk_bf16_f32 v14, v14, v15
	v_cvt_pk_bf16_f32 v15, v16, v17
	v_cvt_pk_bf16_f32 v16, v10, v11
	v_pk_mul_f32 v[10:11], v[12:13], v[18:19]
	s_waitcnt vmcnt(14)
	v_cvt_pk_f32_fp8_e32 v[12:13], v136
	s_mov_b32 s2, 0x58000
	v_cvt_pk_bf16_f32 v17, v10, v11
	v_add_co_u32_e32 v10, vcc, s2, v26
	v_med3_f32 v12, v12, s35, v177
	v_mul_f32_e32 v12, 0xbfb8aa3b, v12
	v_exp_f32_e32 v18, v12
	v_addc_co_u32_e32 v11, vcc, 0, v27, vcc
	v_med3_f32 v12, v13, s35, v177
	global_store_dwordx4 v[10:11], v[14:17], off
	v_mul_f32_e32 v12, 0xbfb8aa3b, v12
	v_exp_f32_e32 v19, v12
	v_cvt_pk_f32_fp8_sdwa v[14:15], v136 src0_sel:WORD_1
	v_cvt_pk_f32_fp8_e32 v[16:17], v137
	v_cvt_pk_f32_fp8_sdwa v[12:13], v137 src0_sel:WORD_1
	v_add_f32_e32 v18, 1.0, v18
	v_med3_f32 v14, v14, s35, v177
	v_med3_f32 v15, v15, s35, v177
	v_med3_f32 v16, v16, s35, v177
	v_med3_f32 v17, v17, s35, v177
	v_mul_f32_e32 v14, 0xbfb8aa3b, v14
	v_mul_f32_e32 v15, 0xbfb8aa3b, v15
	v_mul_f32_e32 v16, 0xbfb8aa3b, v16
	v_mul_f32_e32 v17, 0xbfb8aa3b, v17
	v_med3_f32 v12, v12, s35, v177
	v_med3_f32 v13, v13, s35, v177
	v_exp_f32_e32 v14, v14
	v_exp_f32_e32 v15, v15
	v_exp_f32_e32 v16, v16
	v_exp_f32_e32 v17, v17
	v_mul_f32_e32 v12, 0xbfb8aa3b, v12
	v_mul_f32_e32 v13, 0xbfb8aa3b, v13
	v_exp_f32_e32 v12, v12
	v_exp_f32_e32 v13, v13
	v_add_f32_e32 v19, 1.0, v19
	v_add_f32_e32 v14, 1.0, v14
	v_add_f32_e32 v15, 1.0, v15
	v_add_f32_e32 v16, 1.0, v16
	v_add_f32_e32 v17, 1.0, v17
	v_rcp_f32_e32 v18, v18
	v_rcp_f32_e32 v19, v19
	v_rcp_f32_e32 v14, v14
	v_rcp_f32_e32 v15, v15
	v_rcp_f32_e32 v16, v16
	v_rcp_f32_e32 v17, v17
	v_add_f32_e32 v12, 1.0, v12
	v_add_f32_e32 v13, 1.0, v13
	v_rcp_f32_e32 v12, v12
	v_rcp_f32_e32 v13, v13
	v_pk_mul_f32 v[6:7], v[6:7], v[18:19]
	v_pk_mul_f32 v[8:9], v[8:9], v[14:15]
	v_pk_mul_f32 v[2:3], v[2:3], v[16:17]
	v_cvt_pk_bf16_f32 v6, v6, v7
	v_cvt_pk_bf16_f32 v7, v8, v9
	v_cvt_pk_bf16_f32 v8, v2, v3
	v_pk_mul_f32 v[2:3], v[4:5], v[12:13]
	s_andn2_b64 vcc, exec, s[4:5]
	v_cvt_pk_bf16_f32 v9, v2, v3
	s_mov_b64 s[4:5], -1
	global_store_dwordx4 v[10:11], v[6:9], off offset:256
	s_cbranch_vccnz .LBB0_1038
	s_andn2_b64 vcc, exec, s[12:13]
	s_cbranch_vccnz .LBB0_1037
	s_barrier
	s_branch .LBB0_1037
